# phase 5c (HGRN read-out) rewritten by hand on top of v24: contiguous 1KB accesses, all 8 rows of a wave in flight
# baseline (speedup 1.0000x reference)
; DEV int ltid() { int t = threadIdx.x; asm volatile("" : "+v"(t)); return t; }
; DEV float bflo(unsigned v) { return __uint_as_float(v << 16); }
; DEV float bfhi(unsigned v) { return __uint_as_float(v & 0xffff0000u); }
; DEV void phase5c_rec(CParams& p, int wg, int nwg) {
;   const int wid = ltid() >> 6, lane = ltid() & 63;
;   for (int row = wg * 8 + wid; row < NLAT; row += nwg * 8) {
;     const bf16_t* a = p.of + (long)row * 1024 + lane * 16; const bf16_t* b = p.ob + (long)row * 1024 + lane * 16;
;     const u32x4 a0 = *(const u32x4*)a, a1 = *(const u32x4*)(a + 8), b0 = *(const u32x4*)b, b1 = *(const u32x4*)(b + 8);
;     const unsigned aw[8] = {a0.x, a0.y, a0.z, a0.w, a1.x, a1.y, a1.z, a1.w}, bw[8] = {b0.x, b0.y, b0.z, b0.w, b1.x, b1.y, b1.z, b1.w};
;     float v[16]; float ss = 0.f;
; #pragma unroll
;     for (int i = 0; i < 8; ++i) { v[2 * i] = bflo(aw[i]) + bflo(bw[i]); v[2 * i + 1] = bfhi(aw[i]) + bfhi(bw[i]); ss += v[2 * i] * v[2 * i] + v[2 * i + 1] * v[2 * i + 1]; }
;     ss += __shfl_xor(ss, 1); ss += __shfl_xor(ss, 2); ss += __shfl_xor(ss, 4);
;     const float rstd = rsqrtf(ss * (1.f / DV) + EPS);
;     const bf16_t* gp = p.gate + (long)(NCTX + row) * 1024 + lane * 16;
;     const u32x4 g0 = *(const u32x4*)gp, g1 = *(const u32x4*)(gp + 8);
.LBB0_1183:
	s_or_b64 exec, exec, s[4:5]
	s_mov_b64 s[10:11], s[0:1]
	s_waitcnt lgkmcnt(0)
	v_mov_b32_e32 v1, v0
	s_barrier
	s_mov_b64 s[8:9], exec
	s_load_dwordx4 s[4:7], s[0:1], 0x188
	s_load_dwordx2 s[12:13], s[0:1], 0x198
	s_load_dwordx2 s[14:15], s[0:1], 0x168
	s_load_dwordx2 s[16:17], s[0:1], 0x80
	v_mbcnt_lo_u32_b32 v208, -1, 0
	v_mbcnt_hi_u32_b32 v208, -1, v208
	v_lshlrev_b32_e32 v1, 4, v208
	v_xor_b32_e32 v2, 1, v208
	v_lshlrev_b32_e32 v2, 2, v2
	v_xor_b32_e32 v3, 2, v208
	v_lshlrev_b32_e32 v3, 2, v3
	v_xor_b32_e32 v4, 4, v208
	v_lshlrev_b32_e32 v4, 2, v4
	v_xor_b32_e32 v5, 8, v208
	v_lshlrev_b32_e32 v5, 2, v5
	v_and_b32_e32 v209, 15, v208
	v_lshlrev_b32_e32 v209, 5, v209
	v_lshrrev_b32_e32 v210, 6, v0
	s_nop 0
	v_readfirstlane_b32 s22, v210
	s_nop 3
	s_add_i32 s20, s75, s22
	s_lshl_b32 s21, s33, 3
	s_waitcnt lgkmcnt(0)
	global_load_dwordx4 v[6:9], v209, s[16:17]
	global_load_dwordx4 v[10:13], v209, s[16:17] offset:16
	s_cmp_lt_u32 s20, 0x4000
	s_cbranch_scc0 .Lp5c_end
.Lp5c_chunk:
	s_mov_b32 s23, s20
	s_min_u32 s22, s23, 0x3fff
	s_lshl_b32 s22, s22, 11
	s_add_u32 s24, s6, s22
	s_addc_u32 s25, s7, 0
	s_add_u32 s26, s12, s22
	s_addc_u32 s27, s13, 0
	s_add_u32 s28, s14, s22
	s_addc_u32 s29, s15, 0
	s_add_u32 s28, s28, 0x200000
	s_addc_u32 s29, s29, 0
	global_load_dwordx4 v[16:19], v1, s[24:25] offset:0
	global_load_dwordx4 v[20:23], v1, s[24:25] offset:1024
	global_load_dwordx4 v[24:27], v1, s[26:27] offset:0
	global_load_dwordx4 v[28:31], v1, s[26:27] offset:1024
	global_load_dwordx4 v[32:35], v1, s[28:29] offset:0
	global_load_dwordx4 v[36:39], v1, s[28:29] offset:1024
	s_add_u32 s23, s23, s21
	s_min_u32 s22, s23, 0x3fff
	s_lshl_b32 s22, s22, 11
	s_add_u32 s24, s6, s22
	s_addc_u32 s25, s7, 0
	s_add_u32 s26, s12, s22
	s_addc_u32 s27, s13, 0
	s_add_u32 s28, s14, s22
	s_addc_u32 s29, s15, 0
	s_add_u32 s28, s28, 0x200000
	s_addc_u32 s29, s29, 0
	global_load_dwordx4 v[40:43], v1, s[24:25] offset:0
	global_load_dwordx4 v[44:47], v1, s[24:25] offset:1024
	global_load_dwordx4 v[48:51], v1, s[26:27] offset:0
	global_load_dwordx4 v[52:55], v1, s[26:27] offset:1024
	global_load_dwordx4 v[56:59], v1, s[28:29] offset:0
	global_load_dwordx4 v[60:63], v1, s[28:29] offset:1024
	s_add_u32 s23, s23, s21
	s_min_u32 s22, s23, 0x3fff
	s_lshl_b32 s22, s22, 11
	s_add_u32 s24, s6, s22
	s_addc_u32 s25, s7, 0
	s_add_u32 s26, s12, s22
	s_addc_u32 s27, s13, 0
	s_add_u32 s28, s14, s22
	s_addc_u32 s29, s15, 0
	s_add_u32 s28, s28, 0x200000
	s_addc_u32 s29, s29, 0
	global_load_dwordx4 v[64:67], v1, s[24:25] offset:0
	global_load_dwordx4 v[68:71], v1, s[24:25] offset:1024
	global_load_dwordx4 v[72:75], v1, s[26:27] offset:0
	global_load_dwordx4 v[76:79], v1, s[26:27] offset:1024
	global_load_dwordx4 v[80:83], v1, s[28:29] offset:0
	global_load_dwordx4 v[84:87], v1, s[28:29] offset:1024
	s_add_u32 s23, s23, s21
	s_min_u32 s22, s23, 0x3fff
	s_lshl_b32 s22, s22, 11
	s_add_u32 s24, s6, s22
	s_addc_u32 s25, s7, 0
	s_add_u32 s26, s12, s22
	s_addc_u32 s27, s13, 0
	s_add_u32 s28, s14, s22
	s_addc_u32 s29, s15, 0
	s_add_u32 s28, s28, 0x200000
	s_addc_u32 s29, s29, 0
	global_load_dwordx4 v[88:91], v1, s[24:25] offset:0
	global_load_dwordx4 v[92:95], v1, s[24:25] offset:1024
	global_load_dwordx4 v[96:99], v1, s[26:27] offset:0
	global_load_dwordx4 v[100:103], v1, s[26:27] offset:1024
	global_load_dwordx4 v[104:107], v1, s[28:29] offset:0
	global_load_dwordx4 v[108:111], v1, s[28:29] offset:1024
	s_add_u32 s23, s23, s21
	s_min_u32 s22, s23, 0x3fff
	s_lshl_b32 s22, s22, 11
	s_add_u32 s24, s6, s22
	s_addc_u32 s25, s7, 0
	s_add_u32 s26, s12, s22
	s_addc_u32 s27, s13, 0
	s_add_u32 s28, s14, s22
	s_addc_u32 s29, s15, 0
	s_add_u32 s28, s28, 0x200000
	s_addc_u32 s29, s29, 0
	global_load_dwordx4 v[112:115], v1, s[24:25] offset:0
	global_load_dwordx4 v[116:119], v1, s[24:25] offset:1024
	global_load_dwordx4 v[120:123], v1, s[26:27] offset:0
	global_load_dwordx4 v[124:127], v1, s[26:27] offset:1024
	global_load_dwordx4 v[128:131], v1, s[28:29] offset:0
	global_load_dwordx4 v[132:135], v1, s[28:29] offset:1024
	s_add_u32 s23, s23, s21
	s_min_u32 s22, s23, 0x3fff
	s_lshl_b32 s22, s22, 11
	s_add_u32 s24, s6, s22
	s_addc_u32 s25, s7, 0
	s_add_u32 s26, s12, s22
	s_addc_u32 s27, s13, 0
	s_add_u32 s28, s14, s22
	s_addc_u32 s29, s15, 0
	s_add_u32 s28, s28, 0x200000
	s_addc_u32 s29, s29, 0
	global_load_dwordx4 v[136:139], v1, s[24:25] offset:0
	global_load_dwordx4 v[140:143], v1, s[24:25] offset:1024
	global_load_dwordx4 v[144:147], v1, s[26:27] offset:0
	global_load_dwordx4 v[148:151], v1, s[26:27] offset:1024
	global_load_dwordx4 v[152:155], v1, s[28:29] offset:0
	global_load_dwordx4 v[156:159], v1, s[28:29] offset:1024
	s_add_u32 s23, s23, s21
	s_min_u32 s22, s23, 0x3fff
	s_lshl_b32 s22, s22, 11
	s_add_u32 s24, s6, s22
	s_addc_u32 s25, s7, 0
	s_add_u32 s26, s12, s22
	s_addc_u32 s27, s13, 0
	s_add_u32 s28, s14, s22
	s_addc_u32 s29, s15, 0
	s_add_u32 s28, s28, 0x200000
	s_addc_u32 s29, s29, 0
	global_load_dwordx4 v[160:163], v1, s[24:25] offset:0
	global_load_dwordx4 v[164:167], v1, s[24:25] offset:1024
	global_load_dwordx4 v[168:171], v1, s[26:27] offset:0
	global_load_dwordx4 v[172:175], v1, s[26:27] offset:1024
	global_load_dwordx4 v[176:179], v1, s[28:29] offset:0
	global_load_dwordx4 v[180:183], v1, s[28:29] offset:1024
	s_add_u32 s23, s23, s21
	s_min_u32 s22, s23, 0x3fff
	s_lshl_b32 s22, s22, 11
	s_add_u32 s24, s6, s22
	s_addc_u32 s25, s7, 0
	s_add_u32 s26, s12, s22
	s_addc_u32 s27, s13, 0
	s_add_u32 s28, s14, s22
	s_addc_u32 s29, s15, 0
	s_add_u32 s28, s28, 0x200000
	s_addc_u32 s29, s29, 0
	global_load_dwordx4 v[184:187], v1, s[24:25] offset:0
	global_load_dwordx4 v[188:191], v1, s[24:25] offset:1024
	global_load_dwordx4 v[192:195], v1, s[26:27] offset:0
	global_load_dwordx4 v[196:199], v1, s[26:27] offset:1024
	global_load_dwordx4 v[200:203], v1, s[28:29] offset:0
	global_load_dwordx4 v[204:207], v1, s[28:29] offset:1024
	s_mov_b32 s23, s20
	s_cmp_lt_u32 s23, 0x4000
	s_cbranch_scc0 .Lp5c_end
; DEV unsigned cvt_pk_bf16(float lo, float hi) { const f32x2 v = {lo, hi}; const bf16n2 r = __builtin_convertvector(v, bf16n2); return __builtin_bit_cast(unsigned, r); }
; DEV float bflo(unsigned v) { return __uint_as_float(v << 16); }
; DEV float bfhi(unsigned v) { return __uint_as_float(v & 0xffff0000u); }
; DEV void phase5c_rec(CParams& p, int wg, int nwg) {
;     ...
;     const bf16_t* a = p.of + (long)row * 1024 + lane * 16; const bf16_t* b = p.ob + (long)row * 1024 + lane * 16;
;     const u32x4 a0 = *(const u32x4*)a, a1 = *(const u32x4*)(a + 8), b0 = *(const u32x4*)b, b1 = *(const u32x4*)(b + 8);
;     const unsigned aw[8] = {a0.x, a0.y, a0.z, a0.w, a1.x, a1.y, a1.z, a1.w}, bw[8] = {b0.x, b0.y, b0.z, b0.w, b1.x, b1.y, b1.z, b1.w};
;     float v[16]; float ss = 0.f;
; #pragma unroll
;     for (int i = 0; i < 8; ++i) { v[2 * i] = bflo(aw[i]) + bflo(bw[i]); v[2 * i + 1] = bfhi(aw[i]) + bfhi(bw[i]); ss += v[2 * i] * v[2 * i] + v[2 * i + 1] * v[2 * i + 1]; }
;     ss += __shfl_xor(ss, 1); ss += __shfl_xor(ss, 2); ss += __shfl_xor(ss, 4);
;     const float rstd = rsqrtf(ss * (1.f / DV) + EPS);
;     const bf16_t* gp = p.gate + (long)(NCTX + row) * 1024 + lane * 16;
;     const u32x4 g0 = *(const u32x4*)gp, g1 = *(const u32x4*)(gp + 8);
;     float gt[16]; gt[0] = bflo(g0.x); gt[1] = bfhi(g0.x); gt[2] = bflo(g0.y); gt[3] = bfhi(g0.y); gt[4] = bflo(g0.z); gt[5] = bfhi(g0.z); gt[6] = bflo(g0.w); gt[7] = bfhi(g0.w);
;     gt[8] = bflo(g1.x); gt[9] = bfhi(g1.x); gt[10] = bflo(g1.y); gt[11] = bfhi(g1.y); gt[12] = bflo(g1.z); gt[13] = bfhi(g1.z); gt[14] = bflo(g1.w); gt[15] = bfhi(g1.w);
;     const float* gn = p.g_norm + (lane & 7) * 16;
;     unsigned o[8];
; #pragma unroll
;     for (int j = 0; j < 8; ++j) o[j] = cvt_pk_bf16(v[2 * j] * rstd * gn[2 * j] * gt[2 * j], v[2 * j + 1] * rstd * gn[2 * j + 1] * gt[2 * j + 1]);
;     bf16_t* op = p.aout + (long)row * DM + 1024 + lane * 16;
;     *(u32x4*)op = (u32x4){o[0], o[1], o[2], o[3]}; *(u32x4*)(op + 8) = (u32x4){o[4], o[5], o[6], o[7]};
	s_waitcnt vmcnt(42)
	v_lshlrev_b32_e32 v208, 16, v16
	v_lshlrev_b32_e32 v209, 16, v24
	v_and_b32_e32 v210, 0xffff0000, v16
	v_and_b32_e32 v211, 0xffff0000, v24
	v_add_f32_e32 v16, v208, v209
	v_add_f32_e32 v24, v210, v211
	v_lshlrev_b32_e32 v208, 16, v17
	v_lshlrev_b32_e32 v209, 16, v25
	v_and_b32_e32 v210, 0xffff0000, v17
	v_and_b32_e32 v211, 0xffff0000, v25
	v_add_f32_e32 v17, v208, v209
	v_add_f32_e32 v25, v210, v211
	v_lshlrev_b32_e32 v208, 16, v18
	v_lshlrev_b32_e32 v209, 16, v26
	v_and_b32_e32 v210, 0xffff0000, v18
	v_and_b32_e32 v211, 0xffff0000, v26
	v_add_f32_e32 v18, v208, v209
	v_add_f32_e32 v26, v210, v211
	v_lshlrev_b32_e32 v208, 16, v19
	v_lshlrev_b32_e32 v209, 16, v27
	v_and_b32_e32 v210, 0xffff0000, v19
	v_and_b32_e32 v211, 0xffff0000, v27
	v_add_f32_e32 v19, v208, v209
	v_add_f32_e32 v27, v210, v211
	v_mul_f32_e32 v212, v16, v16
	v_fmac_f32_e32 v212, v24, v24
	v_fmac_f32_e32 v212, v17, v17
	v_fmac_f32_e32 v212, v25, v25
	v_fmac_f32_e32 v212, v18, v18
	v_fmac_f32_e32 v212, v26, v26
	v_fmac_f32_e32 v212, v19, v19
	v_fmac_f32_e32 v212, v27, v27
	v_lshlrev_b32_e32 v208, 16, v20
	v_lshlrev_b32_e32 v209, 16, v28
	v_and_b32_e32 v210, 0xffff0000, v20
	v_and_b32_e32 v211, 0xffff0000, v28
	v_add_f32_e32 v20, v208, v209
	v_add_f32_e32 v28, v210, v211
	v_lshlrev_b32_e32 v208, 16, v21
	v_lshlrev_b32_e32 v209, 16, v29
	v_and_b32_e32 v210, 0xffff0000, v21
	v_and_b32_e32 v211, 0xffff0000, v29
	v_add_f32_e32 v21, v208, v209
	v_add_f32_e32 v29, v210, v211
	v_lshlrev_b32_e32 v208, 16, v22
	v_lshlrev_b32_e32 v209, 16, v30
	v_and_b32_e32 v210, 0xffff0000, v22
	v_and_b32_e32 v211, 0xffff0000, v30
	v_add_f32_e32 v22, v208, v209
	v_add_f32_e32 v30, v210, v211
	v_lshlrev_b32_e32 v208, 16, v23
	v_lshlrev_b32_e32 v209, 16, v31
	v_and_b32_e32 v210, 0xffff0000, v23
	v_and_b32_e32 v211, 0xffff0000, v31
	v_add_f32_e32 v23, v208, v209
	v_add_f32_e32 v31, v210, v211
	v_mul_f32_e32 v213, v20, v20
	v_fmac_f32_e32 v213, v28, v28
	v_fmac_f32_e32 v213, v21, v21
	v_fmac_f32_e32 v213, v29, v29
	v_fmac_f32_e32 v213, v22, v22
	v_fmac_f32_e32 v213, v30, v30
	v_fmac_f32_e32 v213, v23, v23
	v_fmac_f32_e32 v213, v31, v31
	ds_bpermute_b32 v214, v2, v212
	ds_bpermute_b32 v215, v2, v213
	s_waitcnt lgkmcnt(0)
	v_add_f32_e32 v212, v212, v214
	v_add_f32_e32 v213, v213, v215
	ds_bpermute_b32 v214, v3, v212
	ds_bpermute_b32 v215, v3, v213
	s_waitcnt lgkmcnt(0)
	v_add_f32_e32 v212, v212, v214
	v_add_f32_e32 v213, v213, v215
	ds_bpermute_b32 v214, v4, v212
	ds_bpermute_b32 v215, v4, v213
	s_waitcnt lgkmcnt(0)
	v_add_f32_e32 v212, v212, v214
	v_add_f32_e32 v213, v213, v215
	ds_bpermute_b32 v214, v5, v212
	ds_bpermute_b32 v215, v5, v213
	s_waitcnt lgkmcnt(0)
	v_add_f32_e32 v212, v212, v214
	v_add_f32_e32 v213, v213, v215
	v_mov_b32_e32 v214, 0x358637bd
	v_fmac_f32_e32 v214, 0x3c000000, v212
	v_mov_b32_e32 v215, 0x358637bd
	v_fmac_f32_e32 v215, 0x3c000000, v213
	v_rsq_f32_e32 v214, v214
	v_rsq_f32_e32 v215, v215
	s_lshl_b32 s22, s23, 12
	s_add_u32 s30, s4, s22
	s_addc_u32 s31, s5, 0
	v_lshlrev_b32_e32 v208, 16, v32
	v_and_b32_e32 v209, 0xffff0000, v32
	v_mul_f32_e32 v16, v16, v214
	v_mul_f32_e32 v24, v24, v214
	v_mul_f32_e32 v16, v16, v6
	v_mul_f32_e32 v24, v24, v7
	v_mul_f32_e32 v16, v16, v208
	v_mul_f32_e32 v24, v24, v209
	v_cvt_pk_bf16_f32 v32, v16, v24
	v_lshlrev_b32_e32 v208, 16, v33
	v_and_b32_e32 v209, 0xffff0000, v33
	v_mul_f32_e32 v17, v17, v214
	v_mul_f32_e32 v25, v25, v214
	v_mul_f32_e32 v17, v17, v8
	v_mul_f32_e32 v25, v25, v9
	v_mul_f32_e32 v17, v17, v208
	v_mul_f32_e32 v25, v25, v209
	v_cvt_pk_bf16_f32 v33, v17, v25
	v_lshlrev_b32_e32 v208, 16, v34
	v_and_b32_e32 v209, 0xffff0000, v34
	v_mul_f32_e32 v18, v18, v214
	v_mul_f32_e32 v26, v26, v214
	v_mul_f32_e32 v18, v18, v10
	v_mul_f32_e32 v26, v26, v11
	v_mul_f32_e32 v18, v18, v208
	v_mul_f32_e32 v26, v26, v209
	v_cvt_pk_bf16_f32 v34, v18, v26
	v_lshlrev_b32_e32 v208, 16, v35
	v_and_b32_e32 v209, 0xffff0000, v35
	v_mul_f32_e32 v19, v19, v214
	v_mul_f32_e32 v27, v27, v214
	v_mul_f32_e32 v19, v19, v12
	v_mul_f32_e32 v27, v27, v13
	v_mul_f32_e32 v19, v19, v208
	v_mul_f32_e32 v27, v27, v209
	v_cvt_pk_bf16_f32 v35, v19, v27
	global_store_dwordx4 v1, v[32:35], s[30:31] offset:2048
	v_lshlrev_b32_e32 v208, 16, v36
	v_and_b32_e32 v209, 0xffff0000, v36
	v_mul_f32_e32 v20, v20, v215
	v_mul_f32_e32 v28, v28, v215
	v_mul_f32_e32 v20, v20, v6
	v_mul_f32_e32 v28, v28, v7
	v_mul_f32_e32 v20, v20, v208
	v_mul_f32_e32 v28, v28, v209
	v_cvt_pk_bf16_f32 v36, v20, v28
	v_lshlrev_b32_e32 v208, 16, v37
	v_and_b32_e32 v209, 0xffff0000, v37
	v_mul_f32_e32 v21, v21, v215
	v_mul_f32_e32 v29, v29, v215
	v_mul_f32_e32 v21, v21, v8
	v_mul_f32_e32 v29, v29, v9
	v_mul_f32_e32 v21, v21, v208
	v_mul_f32_e32 v29, v29, v209
	v_cvt_pk_bf16_f32 v37, v21, v29
	v_lshlrev_b32_e32 v208, 16, v38
	v_and_b32_e32 v209, 0xffff0000, v38
	v_mul_f32_e32 v22, v22, v215
	v_mul_f32_e32 v30, v30, v215
	v_mul_f32_e32 v22, v22, v10
	v_mul_f32_e32 v30, v30, v11
	v_mul_f32_e32 v22, v22, v208
	v_mul_f32_e32 v30, v30, v209
	v_cvt_pk_bf16_f32 v38, v22, v30
	v_lshlrev_b32_e32 v208, 16, v39
	v_and_b32_e32 v209, 0xffff0000, v39
	v_mul_f32_e32 v23, v23, v215
	v_mul_f32_e32 v31, v31, v215
	v_mul_f32_e32 v23, v23, v12
	v_mul_f32_e32 v31, v31, v13
	v_mul_f32_e32 v23, v23, v208
	v_mul_f32_e32 v31, v31, v209
	v_cvt_pk_bf16_f32 v39, v23, v31
	global_store_dwordx4 v1, v[36:39], s[30:31] offset:3072
	s_add_u32 s23, s23, s21
	s_cmp_lt_u32 s23, 0x4000
	s_cbranch_scc0 .Lp5c_end
; DEV unsigned cvt_pk_bf16(float lo, float hi) { const f32x2 v = {lo, hi}; const bf16n2 r = __builtin_convertvector(v, bf16n2); return __builtin_bit_cast(unsigned, r); }
; DEV float bflo(unsigned v) { return __uint_as_float(v << 16); }
; DEV float bfhi(unsigned v) { return __uint_as_float(v & 0xffff0000u); }
; DEV void phase5c_rec(CParams& p, int wg, int nwg) {
;     ...
;     const bf16_t* a = p.of + (long)row * 1024 + lane * 16; const bf16_t* b = p.ob + (long)row * 1024 + lane * 16;
;     const u32x4 a0 = *(const u32x4*)a, a1 = *(const u32x4*)(a + 8), b0 = *(const u32x4*)b, b1 = *(const u32x4*)(b + 8);
;     const unsigned aw[8] = {a0.x, a0.y, a0.z, a0.w, a1.x, a1.y, a1.z, a1.w}, bw[8] = {b0.x, b0.y, b0.z, b0.w, b1.x, b1.y, b1.z, b1.w};
;     float v[16]; float ss = 0.f;
; #pragma unroll
;     for (int i = 0; i < 8; ++i) { v[2 * i] = bflo(aw[i]) + bflo(bw[i]); v[2 * i + 1] = bfhi(aw[i]) + bfhi(bw[i]); ss += v[2 * i] * v[2 * i] + v[2 * i + 1] * v[2 * i + 1]; }
;     ss += __shfl_xor(ss, 1); ss += __shfl_xor(ss, 2); ss += __shfl_xor(ss, 4);
;     const float rstd = rsqrtf(ss * (1.f / DV) + EPS);
;     const bf16_t* gp = p.gate + (long)(NCTX + row) * 1024 + lane * 16;
;     const u32x4 g0 = *(const u32x4*)gp, g1 = *(const u32x4*)(gp + 8);
;     float gt[16]; gt[0] = bflo(g0.x); gt[1] = bfhi(g0.x); gt[2] = bflo(g0.y); gt[3] = bfhi(g0.y); gt[4] = bflo(g0.z); gt[5] = bfhi(g0.z); gt[6] = bflo(g0.w); gt[7] = bfhi(g0.w);
;     gt[8] = bflo(g1.x); gt[9] = bfhi(g1.x); gt[10] = bflo(g1.y); gt[11] = bfhi(g1.y); gt[12] = bflo(g1.z); gt[13] = bfhi(g1.z); gt[14] = bflo(g1.w); gt[15] = bfhi(g1.w);
;     const float* gn = p.g_norm + (lane & 7) * 16;
;     unsigned o[8];
; #pragma unroll
;     for (int j = 0; j < 8; ++j) o[j] = cvt_pk_bf16(v[2 * j] * rstd * gn[2 * j] * gt[2 * j], v[2 * j + 1] * rstd * gn[2 * j + 1] * gt[2 * j + 1]);
;     bf16_t* op = p.aout + (long)row * DM + 1024 + lane * 16;
;     *(u32x4*)op = (u32x4){o[0], o[1], o[2], o[3]}; *(u32x4*)(op + 8) = (u32x4){o[4], o[5], o[6], o[7]};
	s_waitcnt vmcnt(38)
	v_lshlrev_b32_e32 v208, 16, v40
	v_lshlrev_b32_e32 v209, 16, v48
	v_and_b32_e32 v210, 0xffff0000, v40
	v_and_b32_e32 v211, 0xffff0000, v48
	v_add_f32_e32 v40, v208, v209
	v_add_f32_e32 v48, v210, v211
	v_lshlrev_b32_e32 v208, 16, v41
	v_lshlrev_b32_e32 v209, 16, v49
	v_and_b32_e32 v210, 0xffff0000, v41
	v_and_b32_e32 v211, 0xffff0000, v49
	v_add_f32_e32 v41, v208, v209
	v_add_f32_e32 v49, v210, v211
	v_lshlrev_b32_e32 v208, 16, v42
	v_lshlrev_b32_e32 v209, 16, v50
	v_and_b32_e32 v210, 0xffff0000, v42
	v_and_b32_e32 v211, 0xffff0000, v50
	v_add_f32_e32 v42, v208, v209
	v_add_f32_e32 v50, v210, v211
	v_lshlrev_b32_e32 v208, 16, v43
	v_lshlrev_b32_e32 v209, 16, v51
	v_and_b32_e32 v210, 0xffff0000, v43
	v_and_b32_e32 v211, 0xffff0000, v51
	v_add_f32_e32 v43, v208, v209
	v_add_f32_e32 v51, v210, v211
	v_mul_f32_e32 v212, v40, v40
	v_fmac_f32_e32 v212, v48, v48
	v_fmac_f32_e32 v212, v41, v41
	v_fmac_f32_e32 v212, v49, v49
	v_fmac_f32_e32 v212, v42, v42
	v_fmac_f32_e32 v212, v50, v50
	v_fmac_f32_e32 v212, v43, v43
	v_fmac_f32_e32 v212, v51, v51
	v_lshlrev_b32_e32 v208, 16, v44
	v_lshlrev_b32_e32 v209, 16, v52
	v_and_b32_e32 v210, 0xffff0000, v44
	v_and_b32_e32 v211, 0xffff0000, v52
	v_add_f32_e32 v44, v208, v209
	v_add_f32_e32 v52, v210, v211
	v_lshlrev_b32_e32 v208, 16, v45
	v_lshlrev_b32_e32 v209, 16, v53
	v_and_b32_e32 v210, 0xffff0000, v45
	v_and_b32_e32 v211, 0xffff0000, v53
	v_add_f32_e32 v45, v208, v209
	v_add_f32_e32 v53, v210, v211
	v_lshlrev_b32_e32 v208, 16, v46
	v_lshlrev_b32_e32 v209, 16, v54
	v_and_b32_e32 v210, 0xffff0000, v46
	v_and_b32_e32 v211, 0xffff0000, v54
	v_add_f32_e32 v46, v208, v209
	v_add_f32_e32 v54, v210, v211
	v_lshlrev_b32_e32 v208, 16, v47
	v_lshlrev_b32_e32 v209, 16, v55
	v_and_b32_e32 v210, 0xffff0000, v47
	v_and_b32_e32 v211, 0xffff0000, v55
	v_add_f32_e32 v47, v208, v209
	v_add_f32_e32 v55, v210, v211
	v_mul_f32_e32 v213, v44, v44
	v_fmac_f32_e32 v213, v52, v52
	v_fmac_f32_e32 v213, v45, v45
	v_fmac_f32_e32 v213, v53, v53
	v_fmac_f32_e32 v213, v46, v46
	v_fmac_f32_e32 v213, v54, v54
	v_fmac_f32_e32 v213, v47, v47
	v_fmac_f32_e32 v213, v55, v55
	ds_bpermute_b32 v214, v2, v212
	ds_bpermute_b32 v215, v2, v213
	s_waitcnt lgkmcnt(0)
	v_add_f32_e32 v212, v212, v214
	v_add_f32_e32 v213, v213, v215
	ds_bpermute_b32 v214, v3, v212
	ds_bpermute_b32 v215, v3, v213
	s_waitcnt lgkmcnt(0)
	v_add_f32_e32 v212, v212, v214
	v_add_f32_e32 v213, v213, v215
	ds_bpermute_b32 v214, v4, v212
	ds_bpermute_b32 v215, v4, v213
	s_waitcnt lgkmcnt(0)
	v_add_f32_e32 v212, v212, v214
	v_add_f32_e32 v213, v213, v215
	ds_bpermute_b32 v214, v5, v212
	ds_bpermute_b32 v215, v5, v213
	s_waitcnt lgkmcnt(0)
	v_add_f32_e32 v212, v212, v214
	v_add_f32_e32 v213, v213, v215
	v_mov_b32_e32 v214, 0x358637bd
	v_fmac_f32_e32 v214, 0x3c000000, v212
	v_mov_b32_e32 v215, 0x358637bd
	v_fmac_f32_e32 v215, 0x3c000000, v213
	v_rsq_f32_e32 v214, v214
	v_rsq_f32_e32 v215, v215
	s_lshl_b32 s22, s23, 12
	s_add_u32 s30, s4, s22
	s_addc_u32 s31, s5, 0
	v_lshlrev_b32_e32 v208, 16, v56
	v_and_b32_e32 v209, 0xffff0000, v56
	v_mul_f32_e32 v40, v40, v214
	v_mul_f32_e32 v48, v48, v214
	v_mul_f32_e32 v40, v40, v6
	v_mul_f32_e32 v48, v48, v7
	v_mul_f32_e32 v40, v40, v208
	v_mul_f32_e32 v48, v48, v209
	v_cvt_pk_bf16_f32 v56, v40, v48
	v_lshlrev_b32_e32 v208, 16, v57
	v_and_b32_e32 v209, 0xffff0000, v57
	v_mul_f32_e32 v41, v41, v214
	v_mul_f32_e32 v49, v49, v214
	v_mul_f32_e32 v41, v41, v8
	v_mul_f32_e32 v49, v49, v9
	v_mul_f32_e32 v41, v41, v208
	v_mul_f32_e32 v49, v49, v209
	v_cvt_pk_bf16_f32 v57, v41, v49
	v_lshlrev_b32_e32 v208, 16, v58
	v_and_b32_e32 v209, 0xffff0000, v58
	v_mul_f32_e32 v42, v42, v214
	v_mul_f32_e32 v50, v50, v214
	v_mul_f32_e32 v42, v42, v10
	v_mul_f32_e32 v50, v50, v11
	v_mul_f32_e32 v42, v42, v208
	v_mul_f32_e32 v50, v50, v209
	v_cvt_pk_bf16_f32 v58, v42, v50
	v_lshlrev_b32_e32 v208, 16, v59
	v_and_b32_e32 v209, 0xffff0000, v59
	v_mul_f32_e32 v43, v43, v214
	v_mul_f32_e32 v51, v51, v214
	v_mul_f32_e32 v43, v43, v12
	v_mul_f32_e32 v51, v51, v13
	v_mul_f32_e32 v43, v43, v208
	v_mul_f32_e32 v51, v51, v209
	v_cvt_pk_bf16_f32 v59, v43, v51
	global_store_dwordx4 v1, v[56:59], s[30:31] offset:2048
	v_lshlrev_b32_e32 v208, 16, v60
	v_and_b32_e32 v209, 0xffff0000, v60
	v_mul_f32_e32 v44, v44, v215
	v_mul_f32_e32 v52, v52, v215
	v_mul_f32_e32 v44, v44, v6
	v_mul_f32_e32 v52, v52, v7
	v_mul_f32_e32 v44, v44, v208
	v_mul_f32_e32 v52, v52, v209
	v_cvt_pk_bf16_f32 v60, v44, v52
	v_lshlrev_b32_e32 v208, 16, v61
	v_and_b32_e32 v209, 0xffff0000, v61
	v_mul_f32_e32 v45, v45, v215
	v_mul_f32_e32 v53, v53, v215
	v_mul_f32_e32 v45, v45, v8
	v_mul_f32_e32 v53, v53, v9
	v_mul_f32_e32 v45, v45, v208
	v_mul_f32_e32 v53, v53, v209
	v_cvt_pk_bf16_f32 v61, v45, v53
	v_lshlrev_b32_e32 v208, 16, v62
	v_and_b32_e32 v209, 0xffff0000, v62
	v_mul_f32_e32 v46, v46, v215
	v_mul_f32_e32 v54, v54, v215
	v_mul_f32_e32 v46, v46, v10
	v_mul_f32_e32 v54, v54, v11
	v_mul_f32_e32 v46, v46, v208
	v_mul_f32_e32 v54, v54, v209
	v_cvt_pk_bf16_f32 v62, v46, v54
	v_lshlrev_b32_e32 v208, 16, v63
	v_and_b32_e32 v209, 0xffff0000, v63
	v_mul_f32_e32 v47, v47, v215
	v_mul_f32_e32 v55, v55, v215
	v_mul_f32_e32 v47, v47, v12
	v_mul_f32_e32 v55, v55, v13
	v_mul_f32_e32 v47, v47, v208
	v_mul_f32_e32 v55, v55, v209
	v_cvt_pk_bf16_f32 v63, v47, v55
	global_store_dwordx4 v1, v[60:63], s[30:31] offset:3072
	s_add_u32 s23, s23, s21
	s_cmp_lt_u32 s23, 0x4000
	s_cbranch_scc0 .Lp5c_end
; DEV unsigned cvt_pk_bf16(float lo, float hi) { const f32x2 v = {lo, hi}; const bf16n2 r = __builtin_convertvector(v, bf16n2); return __builtin_bit_cast(unsigned, r); }
; DEV float bflo(unsigned v) { return __uint_as_float(v << 16); }
; DEV float bfhi(unsigned v) { return __uint_as_float(v & 0xffff0000u); }
; DEV void phase5c_rec(CParams& p, int wg, int nwg) {
;     ...
;     const bf16_t* a = p.of + (long)row * 1024 + lane * 16; const bf16_t* b = p.ob + (long)row * 1024 + lane * 16;
;     const u32x4 a0 = *(const u32x4*)a, a1 = *(const u32x4*)(a + 8), b0 = *(const u32x4*)b, b1 = *(const u32x4*)(b + 8);
;     const unsigned aw[8] = {a0.x, a0.y, a0.z, a0.w, a1.x, a1.y, a1.z, a1.w}, bw[8] = {b0.x, b0.y, b0.z, b0.w, b1.x, b1.y, b1.z, b1.w};
;     float v[16]; float ss = 0.f;
; #pragma unroll
;     for (int i = 0; i < 8; ++i) { v[2 * i] = bflo(aw[i]) + bflo(bw[i]); v[2 * i + 1] = bfhi(aw[i]) + bfhi(bw[i]); ss += v[2 * i] * v[2 * i] + v[2 * i + 1] * v[2 * i + 1]; }
;     ss += __shfl_xor(ss, 1); ss += __shfl_xor(ss, 2); ss += __shfl_xor(ss, 4);
;     const float rstd = rsqrtf(ss * (1.f / DV) + EPS);
;     const bf16_t* gp = p.gate + (long)(NCTX + row) * 1024 + lane * 16;
;     const u32x4 g0 = *(const u32x4*)gp, g1 = *(const u32x4*)(gp + 8);
;     float gt[16]; gt[0] = bflo(g0.x); gt[1] = bfhi(g0.x); gt[2] = bflo(g0.y); gt[3] = bfhi(g0.y); gt[4] = bflo(g0.z); gt[5] = bfhi(g0.z); gt[6] = bflo(g0.w); gt[7] = bfhi(g0.w);
;     gt[8] = bflo(g1.x); gt[9] = bfhi(g1.x); gt[10] = bflo(g1.y); gt[11] = bfhi(g1.y); gt[12] = bflo(g1.z); gt[13] = bfhi(g1.z); gt[14] = bflo(g1.w); gt[15] = bfhi(g1.w);
;     const float* gn = p.g_norm + (lane & 7) * 16;
;     unsigned o[8];
; #pragma unroll
;     for (int j = 0; j < 8; ++j) o[j] = cvt_pk_bf16(v[2 * j] * rstd * gn[2 * j] * gt[2 * j], v[2 * j + 1] * rstd * gn[2 * j + 1] * gt[2 * j + 1]);
;     bf16_t* op = p.aout + (long)row * DM + 1024 + lane * 16;
;     *(u32x4*)op = (u32x4){o[0], o[1], o[2], o[3]}; *(u32x4*)(op + 8) = (u32x4){o[4], o[5], o[6], o[7]};
	s_waitcnt vmcnt(34)
	v_lshlrev_b32_e32 v208, 16, v64
	v_lshlrev_b32_e32 v209, 16, v72
	v_and_b32_e32 v210, 0xffff0000, v64
	v_and_b32_e32 v211, 0xffff0000, v72
	v_add_f32_e32 v64, v208, v209
	v_add_f32_e32 v72, v210, v211
	v_lshlrev_b32_e32 v208, 16, v65
	v_lshlrev_b32_e32 v209, 16, v73
	v_and_b32_e32 v210, 0xffff0000, v65
	v_and_b32_e32 v211, 0xffff0000, v73
	v_add_f32_e32 v65, v208, v209
	v_add_f32_e32 v73, v210, v211
	v_lshlrev_b32_e32 v208, 16, v66
	v_lshlrev_b32_e32 v209, 16, v74
	v_and_b32_e32 v210, 0xffff0000, v66
	v_and_b32_e32 v211, 0xffff0000, v74
	v_add_f32_e32 v66, v208, v209
	v_add_f32_e32 v74, v210, v211
	v_lshlrev_b32_e32 v208, 16, v67
	v_lshlrev_b32_e32 v209, 16, v75
	v_and_b32_e32 v210, 0xffff0000, v67
	v_and_b32_e32 v211, 0xffff0000, v75
	v_add_f32_e32 v67, v208, v209
	v_add_f32_e32 v75, v210, v211
	v_mul_f32_e32 v212, v64, v64
	v_fmac_f32_e32 v212, v72, v72
	v_fmac_f32_e32 v212, v65, v65
	v_fmac_f32_e32 v212, v73, v73
	v_fmac_f32_e32 v212, v66, v66
	v_fmac_f32_e32 v212, v74, v74
	v_fmac_f32_e32 v212, v67, v67
	v_fmac_f32_e32 v212, v75, v75
	v_lshlrev_b32_e32 v208, 16, v68
	v_lshlrev_b32_e32 v209, 16, v76
	v_and_b32_e32 v210, 0xffff0000, v68
	v_and_b32_e32 v211, 0xffff0000, v76
	v_add_f32_e32 v68, v208, v209
	v_add_f32_e32 v76, v210, v211
	v_lshlrev_b32_e32 v208, 16, v69
	v_lshlrev_b32_e32 v209, 16, v77
	v_and_b32_e32 v210, 0xffff0000, v69
	v_and_b32_e32 v211, 0xffff0000, v77
	v_add_f32_e32 v69, v208, v209
	v_add_f32_e32 v77, v210, v211
	v_lshlrev_b32_e32 v208, 16, v70
	v_lshlrev_b32_e32 v209, 16, v78
	v_and_b32_e32 v210, 0xffff0000, v70
	v_and_b32_e32 v211, 0xffff0000, v78
	v_add_f32_e32 v70, v208, v209
	v_add_f32_e32 v78, v210, v211
	v_lshlrev_b32_e32 v208, 16, v71
	v_lshlrev_b32_e32 v209, 16, v79
	v_and_b32_e32 v210, 0xffff0000, v71
	v_and_b32_e32 v211, 0xffff0000, v79
	v_add_f32_e32 v71, v208, v209
	v_add_f32_e32 v79, v210, v211
	v_mul_f32_e32 v213, v68, v68
	v_fmac_f32_e32 v213, v76, v76
	v_fmac_f32_e32 v213, v69, v69
	v_fmac_f32_e32 v213, v77, v77
	v_fmac_f32_e32 v213, v70, v70
	v_fmac_f32_e32 v213, v78, v78
	v_fmac_f32_e32 v213, v71, v71
	v_fmac_f32_e32 v213, v79, v79
	ds_bpermute_b32 v214, v2, v212
	ds_bpermute_b32 v215, v2, v213
	s_waitcnt lgkmcnt(0)
	v_add_f32_e32 v212, v212, v214
	v_add_f32_e32 v213, v213, v215
	ds_bpermute_b32 v214, v3, v212
	ds_bpermute_b32 v215, v3, v213
	s_waitcnt lgkmcnt(0)
	v_add_f32_e32 v212, v212, v214
	v_add_f32_e32 v213, v213, v215
	ds_bpermute_b32 v214, v4, v212
	ds_bpermute_b32 v215, v4, v213
	s_waitcnt lgkmcnt(0)
	v_add_f32_e32 v212, v212, v214
	v_add_f32_e32 v213, v213, v215
	ds_bpermute_b32 v214, v5, v212
	ds_bpermute_b32 v215, v5, v213
	s_waitcnt lgkmcnt(0)
	v_add_f32_e32 v212, v212, v214
	v_add_f32_e32 v213, v213, v215
	v_mov_b32_e32 v214, 0x358637bd
	v_fmac_f32_e32 v214, 0x3c000000, v212
	v_mov_b32_e32 v215, 0x358637bd
	v_fmac_f32_e32 v215, 0x3c000000, v213
	v_rsq_f32_e32 v214, v214
	v_rsq_f32_e32 v215, v215
	s_lshl_b32 s22, s23, 12
	s_add_u32 s30, s4, s22
	s_addc_u32 s31, s5, 0
	v_lshlrev_b32_e32 v208, 16, v80
	v_and_b32_e32 v209, 0xffff0000, v80
	v_mul_f32_e32 v64, v64, v214
	v_mul_f32_e32 v72, v72, v214
	v_mul_f32_e32 v64, v64, v6
	v_mul_f32_e32 v72, v72, v7
	v_mul_f32_e32 v64, v64, v208
	v_mul_f32_e32 v72, v72, v209
	v_cvt_pk_bf16_f32 v80, v64, v72
	v_lshlrev_b32_e32 v208, 16, v81
	v_and_b32_e32 v209, 0xffff0000, v81
	v_mul_f32_e32 v65, v65, v214
	v_mul_f32_e32 v73, v73, v214
	v_mul_f32_e32 v65, v65, v8
	v_mul_f32_e32 v73, v73, v9
	v_mul_f32_e32 v65, v65, v208
	v_mul_f32_e32 v73, v73, v209
	v_cvt_pk_bf16_f32 v81, v65, v73
	v_lshlrev_b32_e32 v208, 16, v82
	v_and_b32_e32 v209, 0xffff0000, v82
	v_mul_f32_e32 v66, v66, v214
	v_mul_f32_e32 v74, v74, v214
	v_mul_f32_e32 v66, v66, v10
	v_mul_f32_e32 v74, v74, v11
	v_mul_f32_e32 v66, v66, v208
	v_mul_f32_e32 v74, v74, v209
	v_cvt_pk_bf16_f32 v82, v66, v74
	v_lshlrev_b32_e32 v208, 16, v83
	v_and_b32_e32 v209, 0xffff0000, v83
	v_mul_f32_e32 v67, v67, v214
	v_mul_f32_e32 v75, v75, v214
	v_mul_f32_e32 v67, v67, v12
	v_mul_f32_e32 v75, v75, v13
	v_mul_f32_e32 v67, v67, v208
	v_mul_f32_e32 v75, v75, v209
	v_cvt_pk_bf16_f32 v83, v67, v75
	global_store_dwordx4 v1, v[80:83], s[30:31] offset:2048
	v_lshlrev_b32_e32 v208, 16, v84
	v_and_b32_e32 v209, 0xffff0000, v84
	v_mul_f32_e32 v68, v68, v215
	v_mul_f32_e32 v76, v76, v215
	v_mul_f32_e32 v68, v68, v6
	v_mul_f32_e32 v76, v76, v7
	v_mul_f32_e32 v68, v68, v208
	v_mul_f32_e32 v76, v76, v209
	v_cvt_pk_bf16_f32 v84, v68, v76
	v_lshlrev_b32_e32 v208, 16, v85
	v_and_b32_e32 v209, 0xffff0000, v85
	v_mul_f32_e32 v69, v69, v215
	v_mul_f32_e32 v77, v77, v215
	v_mul_f32_e32 v69, v69, v8
	v_mul_f32_e32 v77, v77, v9
	v_mul_f32_e32 v69, v69, v208
	v_mul_f32_e32 v77, v77, v209
	v_cvt_pk_bf16_f32 v85, v69, v77
	v_lshlrev_b32_e32 v208, 16, v86
	v_and_b32_e32 v209, 0xffff0000, v86
	v_mul_f32_e32 v70, v70, v215
	v_mul_f32_e32 v78, v78, v215
	v_mul_f32_e32 v70, v70, v10
	v_mul_f32_e32 v78, v78, v11
	v_mul_f32_e32 v70, v70, v208
	v_mul_f32_e32 v78, v78, v209
	v_cvt_pk_bf16_f32 v86, v70, v78
	v_lshlrev_b32_e32 v208, 16, v87
	v_and_b32_e32 v209, 0xffff0000, v87
	v_mul_f32_e32 v71, v71, v215
	v_mul_f32_e32 v79, v79, v215
	v_mul_f32_e32 v71, v71, v12
	v_mul_f32_e32 v79, v79, v13
	v_mul_f32_e32 v71, v71, v208
	v_mul_f32_e32 v79, v79, v209
	v_cvt_pk_bf16_f32 v87, v71, v79
	global_store_dwordx4 v1, v[84:87], s[30:31] offset:3072
	s_add_u32 s23, s23, s21
	s_cmp_lt_u32 s23, 0x4000
	s_cbranch_scc0 .Lp5c_end
; DEV unsigned cvt_pk_bf16(float lo, float hi) { const f32x2 v = {lo, hi}; const bf16n2 r = __builtin_convertvector(v, bf16n2); return __builtin_bit_cast(unsigned, r); }
; DEV float bflo(unsigned v) { return __uint_as_float(v << 16); }
; DEV float bfhi(unsigned v) { return __uint_as_float(v & 0xffff0000u); }
; DEV void phase5c_rec(CParams& p, int wg, int nwg) {
;     ...
;     const bf16_t* a = p.of + (long)row * 1024 + lane * 16; const bf16_t* b = p.ob + (long)row * 1024 + lane * 16;
;     const u32x4 a0 = *(const u32x4*)a, a1 = *(const u32x4*)(a + 8), b0 = *(const u32x4*)b, b1 = *(const u32x4*)(b + 8);
;     const unsigned aw[8] = {a0.x, a0.y, a0.z, a0.w, a1.x, a1.y, a1.z, a1.w}, bw[8] = {b0.x, b0.y, b0.z, b0.w, b1.x, b1.y, b1.z, b1.w};
;     float v[16]; float ss = 0.f;
; #pragma unroll
;     for (int i = 0; i < 8; ++i) { v[2 * i] = bflo(aw[i]) + bflo(bw[i]); v[2 * i + 1] = bfhi(aw[i]) + bfhi(bw[i]); ss += v[2 * i] * v[2 * i] + v[2 * i + 1] * v[2 * i + 1]; }
;     ss += __shfl_xor(ss, 1); ss += __shfl_xor(ss, 2); ss += __shfl_xor(ss, 4);
;     const float rstd = rsqrtf(ss * (1.f / DV) + EPS);
;     const bf16_t* gp = p.gate + (long)(NCTX + row) * 1024 + lane * 16;
;     const u32x4 g0 = *(const u32x4*)gp, g1 = *(const u32x4*)(gp + 8);
;     float gt[16]; gt[0] = bflo(g0.x); gt[1] = bfhi(g0.x); gt[2] = bflo(g0.y); gt[3] = bfhi(g0.y); gt[4] = bflo(g0.z); gt[5] = bfhi(g0.z); gt[6] = bflo(g0.w); gt[7] = bfhi(g0.w);
;     gt[8] = bflo(g1.x); gt[9] = bfhi(g1.x); gt[10] = bflo(g1.y); gt[11] = bfhi(g1.y); gt[12] = bflo(g1.z); gt[13] = bfhi(g1.z); gt[14] = bflo(g1.w); gt[15] = bfhi(g1.w);
;     const float* gn = p.g_norm + (lane & 7) * 16;
;     unsigned o[8];
; #pragma unroll
;     for (int j = 0; j < 8; ++j) o[j] = cvt_pk_bf16(v[2 * j] * rstd * gn[2 * j] * gt[2 * j], v[2 * j + 1] * rstd * gn[2 * j + 1] * gt[2 * j + 1]);
;     bf16_t* op = p.aout + (long)row * DM + 1024 + lane * 16;
;     *(u32x4*)op = (u32x4){o[0], o[1], o[2], o[3]}; *(u32x4*)(op + 8) = (u32x4){o[4], o[5], o[6], o[7]};
	s_waitcnt vmcnt(30)
	v_lshlrev_b32_e32 v208, 16, v88
	v_lshlrev_b32_e32 v209, 16, v96
	v_and_b32_e32 v210, 0xffff0000, v88
	v_and_b32_e32 v211, 0xffff0000, v96
	v_add_f32_e32 v88, v208, v209
	v_add_f32_e32 v96, v210, v211
	v_lshlrev_b32_e32 v208, 16, v89
	v_lshlrev_b32_e32 v209, 16, v97
	v_and_b32_e32 v210, 0xffff0000, v89
	v_and_b32_e32 v211, 0xffff0000, v97
	v_add_f32_e32 v89, v208, v209
	v_add_f32_e32 v97, v210, v211
	v_lshlrev_b32_e32 v208, 16, v90
	v_lshlrev_b32_e32 v209, 16, v98
	v_and_b32_e32 v210, 0xffff0000, v90
	v_and_b32_e32 v211, 0xffff0000, v98
	v_add_f32_e32 v90, v208, v209
	v_add_f32_e32 v98, v210, v211
	v_lshlrev_b32_e32 v208, 16, v91
	v_lshlrev_b32_e32 v209, 16, v99
	v_and_b32_e32 v210, 0xffff0000, v91
	v_and_b32_e32 v211, 0xffff0000, v99
	v_add_f32_e32 v91, v208, v209
	v_add_f32_e32 v99, v210, v211
	v_mul_f32_e32 v212, v88, v88
	v_fmac_f32_e32 v212, v96, v96
	v_fmac_f32_e32 v212, v89, v89
	v_fmac_f32_e32 v212, v97, v97
	v_fmac_f32_e32 v212, v90, v90
	v_fmac_f32_e32 v212, v98, v98
	v_fmac_f32_e32 v212, v91, v91
	v_fmac_f32_e32 v212, v99, v99
	v_lshlrev_b32_e32 v208, 16, v92
	v_lshlrev_b32_e32 v209, 16, v100
	v_and_b32_e32 v210, 0xffff0000, v92
	v_and_b32_e32 v211, 0xffff0000, v100
	v_add_f32_e32 v92, v208, v209
	v_add_f32_e32 v100, v210, v211
	v_lshlrev_b32_e32 v208, 16, v93
	v_lshlrev_b32_e32 v209, 16, v101
	v_and_b32_e32 v210, 0xffff0000, v93
	v_and_b32_e32 v211, 0xffff0000, v101
	v_add_f32_e32 v93, v208, v209
	v_add_f32_e32 v101, v210, v211
	v_lshlrev_b32_e32 v208, 16, v94
	v_lshlrev_b32_e32 v209, 16, v102
	v_and_b32_e32 v210, 0xffff0000, v94
	v_and_b32_e32 v211, 0xffff0000, v102
	v_add_f32_e32 v94, v208, v209
	v_add_f32_e32 v102, v210, v211
	v_lshlrev_b32_e32 v208, 16, v95
	v_lshlrev_b32_e32 v209, 16, v103
	v_and_b32_e32 v210, 0xffff0000, v95
	v_and_b32_e32 v211, 0xffff0000, v103
	v_add_f32_e32 v95, v208, v209
	v_add_f32_e32 v103, v210, v211
	v_mul_f32_e32 v213, v92, v92
	v_fmac_f32_e32 v213, v100, v100
	v_fmac_f32_e32 v213, v93, v93
	v_fmac_f32_e32 v213, v101, v101
	v_fmac_f32_e32 v213, v94, v94
	v_fmac_f32_e32 v213, v102, v102
	v_fmac_f32_e32 v213, v95, v95
	v_fmac_f32_e32 v213, v103, v103
	ds_bpermute_b32 v214, v2, v212
	ds_bpermute_b32 v215, v2, v213
	s_waitcnt lgkmcnt(0)
	v_add_f32_e32 v212, v212, v214
	v_add_f32_e32 v213, v213, v215
	ds_bpermute_b32 v214, v3, v212
	ds_bpermute_b32 v215, v3, v213
	s_waitcnt lgkmcnt(0)
	v_add_f32_e32 v212, v212, v214
	v_add_f32_e32 v213, v213, v215
	ds_bpermute_b32 v214, v4, v212
	ds_bpermute_b32 v215, v4, v213
	s_waitcnt lgkmcnt(0)
	v_add_f32_e32 v212, v212, v214
	v_add_f32_e32 v213, v213, v215
	ds_bpermute_b32 v214, v5, v212
	ds_bpermute_b32 v215, v5, v213
	s_waitcnt lgkmcnt(0)
	v_add_f32_e32 v212, v212, v214
	v_add_f32_e32 v213, v213, v215
	v_mov_b32_e32 v214, 0x358637bd
	v_fmac_f32_e32 v214, 0x3c000000, v212
	v_mov_b32_e32 v215, 0x358637bd
	v_fmac_f32_e32 v215, 0x3c000000, v213
	v_rsq_f32_e32 v214, v214
	v_rsq_f32_e32 v215, v215
	s_lshl_b32 s22, s23, 12
	s_add_u32 s30, s4, s22
	s_addc_u32 s31, s5, 0
	v_lshlrev_b32_e32 v208, 16, v104
	v_and_b32_e32 v209, 0xffff0000, v104
	v_mul_f32_e32 v88, v88, v214
	v_mul_f32_e32 v96, v96, v214
	v_mul_f32_e32 v88, v88, v6
	v_mul_f32_e32 v96, v96, v7
	v_mul_f32_e32 v88, v88, v208
	v_mul_f32_e32 v96, v96, v209
	v_cvt_pk_bf16_f32 v104, v88, v96
	v_lshlrev_b32_e32 v208, 16, v105
	v_and_b32_e32 v209, 0xffff0000, v105
	v_mul_f32_e32 v89, v89, v214
	v_mul_f32_e32 v97, v97, v214
	v_mul_f32_e32 v89, v89, v8
	v_mul_f32_e32 v97, v97, v9
	v_mul_f32_e32 v89, v89, v208
	v_mul_f32_e32 v97, v97, v209
	v_cvt_pk_bf16_f32 v105, v89, v97
	v_lshlrev_b32_e32 v208, 16, v106
	v_and_b32_e32 v209, 0xffff0000, v106
	v_mul_f32_e32 v90, v90, v214
	v_mul_f32_e32 v98, v98, v214
	v_mul_f32_e32 v90, v90, v10
	v_mul_f32_e32 v98, v98, v11
	v_mul_f32_e32 v90, v90, v208
	v_mul_f32_e32 v98, v98, v209
	v_cvt_pk_bf16_f32 v106, v90, v98
	v_lshlrev_b32_e32 v208, 16, v107
	v_and_b32_e32 v209, 0xffff0000, v107
	v_mul_f32_e32 v91, v91, v214
	v_mul_f32_e32 v99, v99, v214
	v_mul_f32_e32 v91, v91, v12
	v_mul_f32_e32 v99, v99, v13
	v_mul_f32_e32 v91, v91, v208
	v_mul_f32_e32 v99, v99, v209
	v_cvt_pk_bf16_f32 v107, v91, v99
	global_store_dwordx4 v1, v[104:107], s[30:31] offset:2048
	v_lshlrev_b32_e32 v208, 16, v108
	v_and_b32_e32 v209, 0xffff0000, v108
	v_mul_f32_e32 v92, v92, v215
	v_mul_f32_e32 v100, v100, v215
	v_mul_f32_e32 v92, v92, v6
	v_mul_f32_e32 v100, v100, v7
	v_mul_f32_e32 v92, v92, v208
	v_mul_f32_e32 v100, v100, v209
	v_cvt_pk_bf16_f32 v108, v92, v100
	v_lshlrev_b32_e32 v208, 16, v109
	v_and_b32_e32 v209, 0xffff0000, v109
	v_mul_f32_e32 v93, v93, v215
	v_mul_f32_e32 v101, v101, v215
	v_mul_f32_e32 v93, v93, v8
	v_mul_f32_e32 v101, v101, v9
	v_mul_f32_e32 v93, v93, v208
	v_mul_f32_e32 v101, v101, v209
	v_cvt_pk_bf16_f32 v109, v93, v101
	v_lshlrev_b32_e32 v208, 16, v110
	v_and_b32_e32 v209, 0xffff0000, v110
	v_mul_f32_e32 v94, v94, v215
	v_mul_f32_e32 v102, v102, v215
	v_mul_f32_e32 v94, v94, v10
	v_mul_f32_e32 v102, v102, v11
	v_mul_f32_e32 v94, v94, v208
	v_mul_f32_e32 v102, v102, v209
	v_cvt_pk_bf16_f32 v110, v94, v102
	v_lshlrev_b32_e32 v208, 16, v111
	v_and_b32_e32 v209, 0xffff0000, v111
	v_mul_f32_e32 v95, v95, v215
	v_mul_f32_e32 v103, v103, v215
	v_mul_f32_e32 v95, v95, v12
	v_mul_f32_e32 v103, v103, v13
	v_mul_f32_e32 v95, v95, v208
	v_mul_f32_e32 v103, v103, v209
	v_cvt_pk_bf16_f32 v111, v95, v103
	global_store_dwordx4 v1, v[108:111], s[30:31] offset:3072
	s_add_u32 s23, s23, s21
	s_cmp_lt_u32 s23, 0x4000
	s_cbranch_scc0 .Lp5c_end
; DEV unsigned cvt_pk_bf16(float lo, float hi) { const f32x2 v = {lo, hi}; const bf16n2 r = __builtin_convertvector(v, bf16n2); return __builtin_bit_cast(unsigned, r); }
; DEV float bflo(unsigned v) { return __uint_as_float(v << 16); }
; DEV float bfhi(unsigned v) { return __uint_as_float(v & 0xffff0000u); }
; DEV void phase5c_rec(CParams& p, int wg, int nwg) {
;     ...
;     const bf16_t* a = p.of + (long)row * 1024 + lane * 16; const bf16_t* b = p.ob + (long)row * 1024 + lane * 16;
;     const u32x4 a0 = *(const u32x4*)a, a1 = *(const u32x4*)(a + 8), b0 = *(const u32x4*)b, b1 = *(const u32x4*)(b + 8);
;     const unsigned aw[8] = {a0.x, a0.y, a0.z, a0.w, a1.x, a1.y, a1.z, a1.w}, bw[8] = {b0.x, b0.y, b0.z, b0.w, b1.x, b1.y, b1.z, b1.w};
;     float v[16]; float ss = 0.f;
; #pragma unroll
;     for (int i = 0; i < 8; ++i) { v[2 * i] = bflo(aw[i]) + bflo(bw[i]); v[2 * i + 1] = bfhi(aw[i]) + bfhi(bw[i]); ss += v[2 * i] * v[2 * i] + v[2 * i + 1] * v[2 * i + 1]; }
;     ss += __shfl_xor(ss, 1); ss += __shfl_xor(ss, 2); ss += __shfl_xor(ss, 4);
;     const float rstd = rsqrtf(ss * (1.f / DV) + EPS);
;     const bf16_t* gp = p.gate + (long)(NCTX + row) * 1024 + lane * 16;
;     const u32x4 g0 = *(const u32x4*)gp, g1 = *(const u32x4*)(gp + 8);
;     float gt[16]; gt[0] = bflo(g0.x); gt[1] = bfhi(g0.x); gt[2] = bflo(g0.y); gt[3] = bfhi(g0.y); gt[4] = bflo(g0.z); gt[5] = bfhi(g0.z); gt[6] = bflo(g0.w); gt[7] = bfhi(g0.w);
;     gt[8] = bflo(g1.x); gt[9] = bfhi(g1.x); gt[10] = bflo(g1.y); gt[11] = bfhi(g1.y); gt[12] = bflo(g1.z); gt[13] = bfhi(g1.z); gt[14] = bflo(g1.w); gt[15] = bfhi(g1.w);
;     const float* gn = p.g_norm + (lane & 7) * 16;
;     unsigned o[8];
; #pragma unroll
;     for (int j = 0; j < 8; ++j) o[j] = cvt_pk_bf16(v[2 * j] * rstd * gn[2 * j] * gt[2 * j], v[2 * j + 1] * rstd * gn[2 * j + 1] * gt[2 * j + 1]);
;     bf16_t* op = p.aout + (long)row * DM + 1024 + lane * 16;
;     *(u32x4*)op = (u32x4){o[0], o[1], o[2], o[3]}; *(u32x4*)(op + 8) = (u32x4){o[4], o[5], o[6], o[7]};
	s_waitcnt vmcnt(26)
	v_lshlrev_b32_e32 v208, 16, v112
	v_lshlrev_b32_e32 v209, 16, v120
	v_and_b32_e32 v210, 0xffff0000, v112
	v_and_b32_e32 v211, 0xffff0000, v120
	v_add_f32_e32 v112, v208, v209
	v_add_f32_e32 v120, v210, v211
	v_lshlrev_b32_e32 v208, 16, v113
	v_lshlrev_b32_e32 v209, 16, v121
	v_and_b32_e32 v210, 0xffff0000, v113
	v_and_b32_e32 v211, 0xffff0000, v121
	v_add_f32_e32 v113, v208, v209
	v_add_f32_e32 v121, v210, v211
	v_lshlrev_b32_e32 v208, 16, v114
	v_lshlrev_b32_e32 v209, 16, v122
	v_and_b32_e32 v210, 0xffff0000, v114
	v_and_b32_e32 v211, 0xffff0000, v122
	v_add_f32_e32 v114, v208, v209
	v_add_f32_e32 v122, v210, v211
	v_lshlrev_b32_e32 v208, 16, v115
	v_lshlrev_b32_e32 v209, 16, v123
	v_and_b32_e32 v210, 0xffff0000, v115
	v_and_b32_e32 v211, 0xffff0000, v123
	v_add_f32_e32 v115, v208, v209
	v_add_f32_e32 v123, v210, v211
	v_mul_f32_e32 v212, v112, v112
	v_fmac_f32_e32 v212, v120, v120
	v_fmac_f32_e32 v212, v113, v113
	v_fmac_f32_e32 v212, v121, v121
	v_fmac_f32_e32 v212, v114, v114
	v_fmac_f32_e32 v212, v122, v122
	v_fmac_f32_e32 v212, v115, v115
	v_fmac_f32_e32 v212, v123, v123
	v_lshlrev_b32_e32 v208, 16, v116
	v_lshlrev_b32_e32 v209, 16, v124
	v_and_b32_e32 v210, 0xffff0000, v116
	v_and_b32_e32 v211, 0xffff0000, v124
	v_add_f32_e32 v116, v208, v209
	v_add_f32_e32 v124, v210, v211
	v_lshlrev_b32_e32 v208, 16, v117
	v_lshlrev_b32_e32 v209, 16, v125
	v_and_b32_e32 v210, 0xffff0000, v117
	v_and_b32_e32 v211, 0xffff0000, v125
	v_add_f32_e32 v117, v208, v209
	v_add_f32_e32 v125, v210, v211
	v_lshlrev_b32_e32 v208, 16, v118
	v_lshlrev_b32_e32 v209, 16, v126
	v_and_b32_e32 v210, 0xffff0000, v118
	v_and_b32_e32 v211, 0xffff0000, v126
	v_add_f32_e32 v118, v208, v209
	v_add_f32_e32 v126, v210, v211
	v_lshlrev_b32_e32 v208, 16, v119
	v_lshlrev_b32_e32 v209, 16, v127
	v_and_b32_e32 v210, 0xffff0000, v119
	v_and_b32_e32 v211, 0xffff0000, v127
	v_add_f32_e32 v119, v208, v209
	v_add_f32_e32 v127, v210, v211
	v_mul_f32_e32 v213, v116, v116
	v_fmac_f32_e32 v213, v124, v124
	v_fmac_f32_e32 v213, v117, v117
	v_fmac_f32_e32 v213, v125, v125
	v_fmac_f32_e32 v213, v118, v118
	v_fmac_f32_e32 v213, v126, v126
	v_fmac_f32_e32 v213, v119, v119
	v_fmac_f32_e32 v213, v127, v127
	ds_bpermute_b32 v214, v2, v212
	ds_bpermute_b32 v215, v2, v213
	s_waitcnt lgkmcnt(0)
	v_add_f32_e32 v212, v212, v214
	v_add_f32_e32 v213, v213, v215
	ds_bpermute_b32 v214, v3, v212
	ds_bpermute_b32 v215, v3, v213
	s_waitcnt lgkmcnt(0)
	v_add_f32_e32 v212, v212, v214
	v_add_f32_e32 v213, v213, v215
	ds_bpermute_b32 v214, v4, v212
	ds_bpermute_b32 v215, v4, v213
	s_waitcnt lgkmcnt(0)
	v_add_f32_e32 v212, v212, v214
	v_add_f32_e32 v213, v213, v215
	ds_bpermute_b32 v214, v5, v212
	ds_bpermute_b32 v215, v5, v213
	s_waitcnt lgkmcnt(0)
	v_add_f32_e32 v212, v212, v214
	v_add_f32_e32 v213, v213, v215
	v_mov_b32_e32 v214, 0x358637bd
	v_fmac_f32_e32 v214, 0x3c000000, v212
	v_mov_b32_e32 v215, 0x358637bd
	v_fmac_f32_e32 v215, 0x3c000000, v213
	v_rsq_f32_e32 v214, v214
	v_rsq_f32_e32 v215, v215
	s_lshl_b32 s22, s23, 12
	s_add_u32 s30, s4, s22
	s_addc_u32 s31, s5, 0
	v_lshlrev_b32_e32 v208, 16, v128
	v_and_b32_e32 v209, 0xffff0000, v128
	v_mul_f32_e32 v112, v112, v214
	v_mul_f32_e32 v120, v120, v214
	v_mul_f32_e32 v112, v112, v6
	v_mul_f32_e32 v120, v120, v7
	v_mul_f32_e32 v112, v112, v208
	v_mul_f32_e32 v120, v120, v209
	v_cvt_pk_bf16_f32 v128, v112, v120
	v_lshlrev_b32_e32 v208, 16, v129
	v_and_b32_e32 v209, 0xffff0000, v129
	v_mul_f32_e32 v113, v113, v214
	v_mul_f32_e32 v121, v121, v214
	v_mul_f32_e32 v113, v113, v8
	v_mul_f32_e32 v121, v121, v9
	v_mul_f32_e32 v113, v113, v208
	v_mul_f32_e32 v121, v121, v209
	v_cvt_pk_bf16_f32 v129, v113, v121
	v_lshlrev_b32_e32 v208, 16, v130
	v_and_b32_e32 v209, 0xffff0000, v130
	v_mul_f32_e32 v114, v114, v214
	v_mul_f32_e32 v122, v122, v214
	v_mul_f32_e32 v114, v114, v10
	v_mul_f32_e32 v122, v122, v11
	v_mul_f32_e32 v114, v114, v208
	v_mul_f32_e32 v122, v122, v209
	v_cvt_pk_bf16_f32 v130, v114, v122
	v_lshlrev_b32_e32 v208, 16, v131
	v_and_b32_e32 v209, 0xffff0000, v131
	v_mul_f32_e32 v115, v115, v214
	v_mul_f32_e32 v123, v123, v214
	v_mul_f32_e32 v115, v115, v12
	v_mul_f32_e32 v123, v123, v13
	v_mul_f32_e32 v115, v115, v208
	v_mul_f32_e32 v123, v123, v209
	v_cvt_pk_bf16_f32 v131, v115, v123
	global_store_dwordx4 v1, v[128:131], s[30:31] offset:2048
	v_lshlrev_b32_e32 v208, 16, v132
	v_and_b32_e32 v209, 0xffff0000, v132
	v_mul_f32_e32 v116, v116, v215
	v_mul_f32_e32 v124, v124, v215
	v_mul_f32_e32 v116, v116, v6
	v_mul_f32_e32 v124, v124, v7
	v_mul_f32_e32 v116, v116, v208
	v_mul_f32_e32 v124, v124, v209
	v_cvt_pk_bf16_f32 v132, v116, v124
	v_lshlrev_b32_e32 v208, 16, v133
	v_and_b32_e32 v209, 0xffff0000, v133
	v_mul_f32_e32 v117, v117, v215
	v_mul_f32_e32 v125, v125, v215
	v_mul_f32_e32 v117, v117, v8
	v_mul_f32_e32 v125, v125, v9
	v_mul_f32_e32 v117, v117, v208
	v_mul_f32_e32 v125, v125, v209
	v_cvt_pk_bf16_f32 v133, v117, v125
	v_lshlrev_b32_e32 v208, 16, v134
	v_and_b32_e32 v209, 0xffff0000, v134
	v_mul_f32_e32 v118, v118, v215
	v_mul_f32_e32 v126, v126, v215
	v_mul_f32_e32 v118, v118, v10
	v_mul_f32_e32 v126, v126, v11
	v_mul_f32_e32 v118, v118, v208
	v_mul_f32_e32 v126, v126, v209
	v_cvt_pk_bf16_f32 v134, v118, v126
	v_lshlrev_b32_e32 v208, 16, v135
	v_and_b32_e32 v209, 0xffff0000, v135
	v_mul_f32_e32 v119, v119, v215
	v_mul_f32_e32 v127, v127, v215
	v_mul_f32_e32 v119, v119, v12
	v_mul_f32_e32 v127, v127, v13
	v_mul_f32_e32 v119, v119, v208
	v_mul_f32_e32 v127, v127, v209
	v_cvt_pk_bf16_f32 v135, v119, v127
	global_store_dwordx4 v1, v[132:135], s[30:31] offset:3072
	s_add_u32 s23, s23, s21
	s_cmp_lt_u32 s23, 0x4000
	s_cbranch_scc0 .Lp5c_end
; DEV unsigned cvt_pk_bf16(float lo, float hi) { const f32x2 v = {lo, hi}; const bf16n2 r = __builtin_convertvector(v, bf16n2); return __builtin_bit_cast(unsigned, r); }
; DEV float bflo(unsigned v) { return __uint_as_float(v << 16); }
; DEV float bfhi(unsigned v) { return __uint_as_float(v & 0xffff0000u); }
; DEV void phase5c_rec(CParams& p, int wg, int nwg) {
;     ...
;     const bf16_t* a = p.of + (long)row * 1024 + lane * 16; const bf16_t* b = p.ob + (long)row * 1024 + lane * 16;
;     const u32x4 a0 = *(const u32x4*)a, a1 = *(const u32x4*)(a + 8), b0 = *(const u32x4*)b, b1 = *(const u32x4*)(b + 8);
;     const unsigned aw[8] = {a0.x, a0.y, a0.z, a0.w, a1.x, a1.y, a1.z, a1.w}, bw[8] = {b0.x, b0.y, b0.z, b0.w, b1.x, b1.y, b1.z, b1.w};
;     float v[16]; float ss = 0.f;
; #pragma unroll
;     for (int i = 0; i < 8; ++i) { v[2 * i] = bflo(aw[i]) + bflo(bw[i]); v[2 * i + 1] = bfhi(aw[i]) + bfhi(bw[i]); ss += v[2 * i] * v[2 * i] + v[2 * i + 1] * v[2 * i + 1]; }
;     ss += __shfl_xor(ss, 1); ss += __shfl_xor(ss, 2); ss += __shfl_xor(ss, 4);
;     const float rstd = rsqrtf(ss * (1.f / DV) + EPS);
;     const bf16_t* gp = p.gate + (long)(NCTX + row) * 1024 + lane * 16;
;     const u32x4 g0 = *(const u32x4*)gp, g1 = *(const u32x4*)(gp + 8);
;     float gt[16]; gt[0] = bflo(g0.x); gt[1] = bfhi(g0.x); gt[2] = bflo(g0.y); gt[3] = bfhi(g0.y); gt[4] = bflo(g0.z); gt[5] = bfhi(g0.z); gt[6] = bflo(g0.w); gt[7] = bfhi(g0.w);
;     gt[8] = bflo(g1.x); gt[9] = bfhi(g1.x); gt[10] = bflo(g1.y); gt[11] = bfhi(g1.y); gt[12] = bflo(g1.z); gt[13] = bfhi(g1.z); gt[14] = bflo(g1.w); gt[15] = bfhi(g1.w);
;     const float* gn = p.g_norm + (lane & 7) * 16;
;     unsigned o[8];
; #pragma unroll
;     for (int j = 0; j < 8; ++j) o[j] = cvt_pk_bf16(v[2 * j] * rstd * gn[2 * j] * gt[2 * j], v[2 * j + 1] * rstd * gn[2 * j + 1] * gt[2 * j + 1]);
;     bf16_t* op = p.aout + (long)row * DM + 1024 + lane * 16;
;     *(u32x4*)op = (u32x4){o[0], o[1], o[2], o[3]}; *(u32x4*)(op + 8) = (u32x4){o[4], o[5], o[6], o[7]};
	s_waitcnt vmcnt(22)
	v_lshlrev_b32_e32 v208, 16, v136
	v_lshlrev_b32_e32 v209, 16, v144
	v_and_b32_e32 v210, 0xffff0000, v136
	v_and_b32_e32 v211, 0xffff0000, v144
	v_add_f32_e32 v136, v208, v209
	v_add_f32_e32 v144, v210, v211
	v_lshlrev_b32_e32 v208, 16, v137
	v_lshlrev_b32_e32 v209, 16, v145
	v_and_b32_e32 v210, 0xffff0000, v137
	v_and_b32_e32 v211, 0xffff0000, v145
	v_add_f32_e32 v137, v208, v209
	v_add_f32_e32 v145, v210, v211
	v_lshlrev_b32_e32 v208, 16, v138
	v_lshlrev_b32_e32 v209, 16, v146
	v_and_b32_e32 v210, 0xffff0000, v138
	v_and_b32_e32 v211, 0xffff0000, v146
	v_add_f32_e32 v138, v208, v209
	v_add_f32_e32 v146, v210, v211
	v_lshlrev_b32_e32 v208, 16, v139
	v_lshlrev_b32_e32 v209, 16, v147
	v_and_b32_e32 v210, 0xffff0000, v139
	v_and_b32_e32 v211, 0xffff0000, v147
	v_add_f32_e32 v139, v208, v209
	v_add_f32_e32 v147, v210, v211
	v_mul_f32_e32 v212, v136, v136
	v_fmac_f32_e32 v212, v144, v144
	v_fmac_f32_e32 v212, v137, v137
	v_fmac_f32_e32 v212, v145, v145
	v_fmac_f32_e32 v212, v138, v138
	v_fmac_f32_e32 v212, v146, v146
	v_fmac_f32_e32 v212, v139, v139
	v_fmac_f32_e32 v212, v147, v147
	v_lshlrev_b32_e32 v208, 16, v140
	v_lshlrev_b32_e32 v209, 16, v148
	v_and_b32_e32 v210, 0xffff0000, v140
	v_and_b32_e32 v211, 0xffff0000, v148
	v_add_f32_e32 v140, v208, v209
	v_add_f32_e32 v148, v210, v211
	v_lshlrev_b32_e32 v208, 16, v141
	v_lshlrev_b32_e32 v209, 16, v149
	v_and_b32_e32 v210, 0xffff0000, v141
	v_and_b32_e32 v211, 0xffff0000, v149
	v_add_f32_e32 v141, v208, v209
	v_add_f32_e32 v149, v210, v211
	v_lshlrev_b32_e32 v208, 16, v142
	v_lshlrev_b32_e32 v209, 16, v150
	v_and_b32_e32 v210, 0xffff0000, v142
	v_and_b32_e32 v211, 0xffff0000, v150
	v_add_f32_e32 v142, v208, v209
	v_add_f32_e32 v150, v210, v211
	v_lshlrev_b32_e32 v208, 16, v143
	v_lshlrev_b32_e32 v209, 16, v151
	v_and_b32_e32 v210, 0xffff0000, v143
	v_and_b32_e32 v211, 0xffff0000, v151
	v_add_f32_e32 v143, v208, v209
	v_add_f32_e32 v151, v210, v211
	v_mul_f32_e32 v213, v140, v140
	v_fmac_f32_e32 v213, v148, v148
	v_fmac_f32_e32 v213, v141, v141
	v_fmac_f32_e32 v213, v149, v149
	v_fmac_f32_e32 v213, v142, v142
	v_fmac_f32_e32 v213, v150, v150
	v_fmac_f32_e32 v213, v143, v143
	v_fmac_f32_e32 v213, v151, v151
	ds_bpermute_b32 v214, v2, v212
	ds_bpermute_b32 v215, v2, v213
	s_waitcnt lgkmcnt(0)
	v_add_f32_e32 v212, v212, v214
	v_add_f32_e32 v213, v213, v215
	ds_bpermute_b32 v214, v3, v212
	ds_bpermute_b32 v215, v3, v213
	s_waitcnt lgkmcnt(0)
	v_add_f32_e32 v212, v212, v214
	v_add_f32_e32 v213, v213, v215
	ds_bpermute_b32 v214, v4, v212
	ds_bpermute_b32 v215, v4, v213
	s_waitcnt lgkmcnt(0)
	v_add_f32_e32 v212, v212, v214
	v_add_f32_e32 v213, v213, v215
	ds_bpermute_b32 v214, v5, v212
	ds_bpermute_b32 v215, v5, v213
	s_waitcnt lgkmcnt(0)
	v_add_f32_e32 v212, v212, v214
	v_add_f32_e32 v213, v213, v215
	v_mov_b32_e32 v214, 0x358637bd
	v_fmac_f32_e32 v214, 0x3c000000, v212
	v_mov_b32_e32 v215, 0x358637bd
	v_fmac_f32_e32 v215, 0x3c000000, v213
	v_rsq_f32_e32 v214, v214
	v_rsq_f32_e32 v215, v215
	s_lshl_b32 s22, s23, 12
	s_add_u32 s30, s4, s22
	s_addc_u32 s31, s5, 0
	v_lshlrev_b32_e32 v208, 16, v152
	v_and_b32_e32 v209, 0xffff0000, v152
	v_mul_f32_e32 v136, v136, v214
	v_mul_f32_e32 v144, v144, v214
	v_mul_f32_e32 v136, v136, v6
	v_mul_f32_e32 v144, v144, v7
	v_mul_f32_e32 v136, v136, v208
	v_mul_f32_e32 v144, v144, v209
	v_cvt_pk_bf16_f32 v152, v136, v144
	v_lshlrev_b32_e32 v208, 16, v153
	v_and_b32_e32 v209, 0xffff0000, v153
	v_mul_f32_e32 v137, v137, v214
	v_mul_f32_e32 v145, v145, v214
	v_mul_f32_e32 v137, v137, v8
	v_mul_f32_e32 v145, v145, v9
	v_mul_f32_e32 v137, v137, v208
	v_mul_f32_e32 v145, v145, v209
	v_cvt_pk_bf16_f32 v153, v137, v145
	v_lshlrev_b32_e32 v208, 16, v154
	v_and_b32_e32 v209, 0xffff0000, v154
	v_mul_f32_e32 v138, v138, v214
	v_mul_f32_e32 v146, v146, v214
	v_mul_f32_e32 v138, v138, v10
	v_mul_f32_e32 v146, v146, v11
	v_mul_f32_e32 v138, v138, v208
	v_mul_f32_e32 v146, v146, v209
	v_cvt_pk_bf16_f32 v154, v138, v146
	v_lshlrev_b32_e32 v208, 16, v155
	v_and_b32_e32 v209, 0xffff0000, v155
	v_mul_f32_e32 v139, v139, v214
	v_mul_f32_e32 v147, v147, v214
	v_mul_f32_e32 v139, v139, v12
	v_mul_f32_e32 v147, v147, v13
	v_mul_f32_e32 v139, v139, v208
	v_mul_f32_e32 v147, v147, v209
	v_cvt_pk_bf16_f32 v155, v139, v147
	global_store_dwordx4 v1, v[152:155], s[30:31] offset:2048
	v_lshlrev_b32_e32 v208, 16, v156
	v_and_b32_e32 v209, 0xffff0000, v156
	v_mul_f32_e32 v140, v140, v215
	v_mul_f32_e32 v148, v148, v215
	v_mul_f32_e32 v140, v140, v6
	v_mul_f32_e32 v148, v148, v7
	v_mul_f32_e32 v140, v140, v208
	v_mul_f32_e32 v148, v148, v209
	v_cvt_pk_bf16_f32 v156, v140, v148
	v_lshlrev_b32_e32 v208, 16, v157
	v_and_b32_e32 v209, 0xffff0000, v157
	v_mul_f32_e32 v141, v141, v215
	v_mul_f32_e32 v149, v149, v215
	v_mul_f32_e32 v141, v141, v8
	v_mul_f32_e32 v149, v149, v9
	v_mul_f32_e32 v141, v141, v208
	v_mul_f32_e32 v149, v149, v209
	v_cvt_pk_bf16_f32 v157, v141, v149
	v_lshlrev_b32_e32 v208, 16, v158
	v_and_b32_e32 v209, 0xffff0000, v158
	v_mul_f32_e32 v142, v142, v215
	v_mul_f32_e32 v150, v150, v215
	v_mul_f32_e32 v142, v142, v10
	v_mul_f32_e32 v150, v150, v11
	v_mul_f32_e32 v142, v142, v208
	v_mul_f32_e32 v150, v150, v209
	v_cvt_pk_bf16_f32 v158, v142, v150
	v_lshlrev_b32_e32 v208, 16, v159
	v_and_b32_e32 v209, 0xffff0000, v159
	v_mul_f32_e32 v143, v143, v215
	v_mul_f32_e32 v151, v151, v215
	v_mul_f32_e32 v143, v143, v12
	v_mul_f32_e32 v151, v151, v13
	v_mul_f32_e32 v143, v143, v208
	v_mul_f32_e32 v151, v151, v209
	v_cvt_pk_bf16_f32 v159, v143, v151
	global_store_dwordx4 v1, v[156:159], s[30:31] offset:3072
	s_add_u32 s23, s23, s21
	s_cmp_lt_u32 s23, 0x4000
	s_cbranch_scc0 .Lp5c_end
; DEV unsigned cvt_pk_bf16(float lo, float hi) { const f32x2 v = {lo, hi}; const bf16n2 r = __builtin_convertvector(v, bf16n2); return __builtin_bit_cast(unsigned, r); }
; DEV float bflo(unsigned v) { return __uint_as_float(v << 16); }
; DEV float bfhi(unsigned v) { return __uint_as_float(v & 0xffff0000u); }
; DEV void phase5c_rec(CParams& p, int wg, int nwg) {
;     ...
;     const bf16_t* a = p.of + (long)row * 1024 + lane * 16; const bf16_t* b = p.ob + (long)row * 1024 + lane * 16;
;     const u32x4 a0 = *(const u32x4*)a, a1 = *(const u32x4*)(a + 8), b0 = *(const u32x4*)b, b1 = *(const u32x4*)(b + 8);
;     const unsigned aw[8] = {a0.x, a0.y, a0.z, a0.w, a1.x, a1.y, a1.z, a1.w}, bw[8] = {b0.x, b0.y, b0.z, b0.w, b1.x, b1.y, b1.z, b1.w};
;     float v[16]; float ss = 0.f;
; #pragma unroll
;     for (int i = 0; i < 8; ++i) { v[2 * i] = bflo(aw[i]) + bflo(bw[i]); v[2 * i + 1] = bfhi(aw[i]) + bfhi(bw[i]); ss += v[2 * i] * v[2 * i] + v[2 * i + 1] * v[2 * i + 1]; }
;     ss += __shfl_xor(ss, 1); ss += __shfl_xor(ss, 2); ss += __shfl_xor(ss, 4);
;     const float rstd = rsqrtf(ss * (1.f / DV) + EPS);
;     const bf16_t* gp = p.gate + (long)(NCTX + row) * 1024 + lane * 16;
;     const u32x4 g0 = *(const u32x4*)gp, g1 = *(const u32x4*)(gp + 8);
;     float gt[16]; gt[0] = bflo(g0.x); gt[1] = bfhi(g0.x); gt[2] = bflo(g0.y); gt[3] = bfhi(g0.y); gt[4] = bflo(g0.z); gt[5] = bfhi(g0.z); gt[6] = bflo(g0.w); gt[7] = bfhi(g0.w);
;     gt[8] = bflo(g1.x); gt[9] = bfhi(g1.x); gt[10] = bflo(g1.y); gt[11] = bfhi(g1.y); gt[12] = bflo(g1.z); gt[13] = bfhi(g1.z); gt[14] = bflo(g1.w); gt[15] = bfhi(g1.w);
;     const float* gn = p.g_norm + (lane & 7) * 16;
;     unsigned o[8];
; #pragma unroll
;     for (int j = 0; j < 8; ++j) o[j] = cvt_pk_bf16(v[2 * j] * rstd * gn[2 * j] * gt[2 * j], v[2 * j + 1] * rstd * gn[2 * j + 1] * gt[2 * j + 1]);
;     bf16_t* op = p.aout + (long)row * DM + 1024 + lane * 16;
;     *(u32x4*)op = (u32x4){o[0], o[1], o[2], o[3]}; *(u32x4*)(op + 8) = (u32x4){o[4], o[5], o[6], o[7]};
	s_waitcnt vmcnt(18)
	v_lshlrev_b32_e32 v208, 16, v160
	v_lshlrev_b32_e32 v209, 16, v168
	v_and_b32_e32 v210, 0xffff0000, v160
	v_and_b32_e32 v211, 0xffff0000, v168
	v_add_f32_e32 v160, v208, v209
	v_add_f32_e32 v168, v210, v211
	v_lshlrev_b32_e32 v208, 16, v161
	v_lshlrev_b32_e32 v209, 16, v169
	v_and_b32_e32 v210, 0xffff0000, v161
	v_and_b32_e32 v211, 0xffff0000, v169
	v_add_f32_e32 v161, v208, v209
	v_add_f32_e32 v169, v210, v211
	v_lshlrev_b32_e32 v208, 16, v162
	v_lshlrev_b32_e32 v209, 16, v170
	v_and_b32_e32 v210, 0xffff0000, v162
	v_and_b32_e32 v211, 0xffff0000, v170
	v_add_f32_e32 v162, v208, v209
	v_add_f32_e32 v170, v210, v211
	v_lshlrev_b32_e32 v208, 16, v163
	v_lshlrev_b32_e32 v209, 16, v171
	v_and_b32_e32 v210, 0xffff0000, v163
	v_and_b32_e32 v211, 0xffff0000, v171
	v_add_f32_e32 v163, v208, v209
	v_add_f32_e32 v171, v210, v211
	v_mul_f32_e32 v212, v160, v160
	v_fmac_f32_e32 v212, v168, v168
	v_fmac_f32_e32 v212, v161, v161
	v_fmac_f32_e32 v212, v169, v169
	v_fmac_f32_e32 v212, v162, v162
	v_fmac_f32_e32 v212, v170, v170
	v_fmac_f32_e32 v212, v163, v163
	v_fmac_f32_e32 v212, v171, v171
	v_lshlrev_b32_e32 v208, 16, v164
	v_lshlrev_b32_e32 v209, 16, v172
	v_and_b32_e32 v210, 0xffff0000, v164
	v_and_b32_e32 v211, 0xffff0000, v172
	v_add_f32_e32 v164, v208, v209
	v_add_f32_e32 v172, v210, v211
	v_lshlrev_b32_e32 v208, 16, v165
	v_lshlrev_b32_e32 v209, 16, v173
	v_and_b32_e32 v210, 0xffff0000, v165
	v_and_b32_e32 v211, 0xffff0000, v173
	v_add_f32_e32 v165, v208, v209
	v_add_f32_e32 v173, v210, v211
	v_lshlrev_b32_e32 v208, 16, v166
	v_lshlrev_b32_e32 v209, 16, v174
	v_and_b32_e32 v210, 0xffff0000, v166
	v_and_b32_e32 v211, 0xffff0000, v174
	v_add_f32_e32 v166, v208, v209
	v_add_f32_e32 v174, v210, v211
	v_lshlrev_b32_e32 v208, 16, v167
	v_lshlrev_b32_e32 v209, 16, v175
	v_and_b32_e32 v210, 0xffff0000, v167
	v_and_b32_e32 v211, 0xffff0000, v175
	v_add_f32_e32 v167, v208, v209
	v_add_f32_e32 v175, v210, v211
	v_mul_f32_e32 v213, v164, v164
	v_fmac_f32_e32 v213, v172, v172
	v_fmac_f32_e32 v213, v165, v165
	v_fmac_f32_e32 v213, v173, v173
	v_fmac_f32_e32 v213, v166, v166
	v_fmac_f32_e32 v213, v174, v174
	v_fmac_f32_e32 v213, v167, v167
	v_fmac_f32_e32 v213, v175, v175
	ds_bpermute_b32 v214, v2, v212
	ds_bpermute_b32 v215, v2, v213
	s_waitcnt lgkmcnt(0)
	v_add_f32_e32 v212, v212, v214
	v_add_f32_e32 v213, v213, v215
	ds_bpermute_b32 v214, v3, v212
	ds_bpermute_b32 v215, v3, v213
	s_waitcnt lgkmcnt(0)
	v_add_f32_e32 v212, v212, v214
	v_add_f32_e32 v213, v213, v215
	ds_bpermute_b32 v214, v4, v212
	ds_bpermute_b32 v215, v4, v213
	s_waitcnt lgkmcnt(0)
	v_add_f32_e32 v212, v212, v214
	v_add_f32_e32 v213, v213, v215
	ds_bpermute_b32 v214, v5, v212
	ds_bpermute_b32 v215, v5, v213
	s_waitcnt lgkmcnt(0)
	v_add_f32_e32 v212, v212, v214
	v_add_f32_e32 v213, v213, v215
	v_mov_b32_e32 v214, 0x358637bd
	v_fmac_f32_e32 v214, 0x3c000000, v212
	v_mov_b32_e32 v215, 0x358637bd
	v_fmac_f32_e32 v215, 0x3c000000, v213
	v_rsq_f32_e32 v214, v214
	v_rsq_f32_e32 v215, v215
	s_lshl_b32 s22, s23, 12
	s_add_u32 s30, s4, s22
	s_addc_u32 s31, s5, 0
	v_lshlrev_b32_e32 v208, 16, v176
	v_and_b32_e32 v209, 0xffff0000, v176
	v_mul_f32_e32 v160, v160, v214
	v_mul_f32_e32 v168, v168, v214
	v_mul_f32_e32 v160, v160, v6
	v_mul_f32_e32 v168, v168, v7
	v_mul_f32_e32 v160, v160, v208
	v_mul_f32_e32 v168, v168, v209
	v_cvt_pk_bf16_f32 v176, v160, v168
	v_lshlrev_b32_e32 v208, 16, v177
	v_and_b32_e32 v209, 0xffff0000, v177
	v_mul_f32_e32 v161, v161, v214
	v_mul_f32_e32 v169, v169, v214
	v_mul_f32_e32 v161, v161, v8
	v_mul_f32_e32 v169, v169, v9
	v_mul_f32_e32 v161, v161, v208
	v_mul_f32_e32 v169, v169, v209
	v_cvt_pk_bf16_f32 v177, v161, v169
	v_lshlrev_b32_e32 v208, 16, v178
	v_and_b32_e32 v209, 0xffff0000, v178
	v_mul_f32_e32 v162, v162, v214
	v_mul_f32_e32 v170, v170, v214
	v_mul_f32_e32 v162, v162, v10
	v_mul_f32_e32 v170, v170, v11
	v_mul_f32_e32 v162, v162, v208
	v_mul_f32_e32 v170, v170, v209
	v_cvt_pk_bf16_f32 v178, v162, v170
	v_lshlrev_b32_e32 v208, 16, v179
	v_and_b32_e32 v209, 0xffff0000, v179
	v_mul_f32_e32 v163, v163, v214
	v_mul_f32_e32 v171, v171, v214
	v_mul_f32_e32 v163, v163, v12
	v_mul_f32_e32 v171, v171, v13
	v_mul_f32_e32 v163, v163, v208
	v_mul_f32_e32 v171, v171, v209
	v_cvt_pk_bf16_f32 v179, v163, v171
	global_store_dwordx4 v1, v[176:179], s[30:31] offset:2048
	v_lshlrev_b32_e32 v208, 16, v180
	v_and_b32_e32 v209, 0xffff0000, v180
	v_mul_f32_e32 v164, v164, v215
	v_mul_f32_e32 v172, v172, v215
	v_mul_f32_e32 v164, v164, v6
	v_mul_f32_e32 v172, v172, v7
	v_mul_f32_e32 v164, v164, v208
	v_mul_f32_e32 v172, v172, v209
	v_cvt_pk_bf16_f32 v180, v164, v172
	v_lshlrev_b32_e32 v208, 16, v181
	v_and_b32_e32 v209, 0xffff0000, v181
	v_mul_f32_e32 v165, v165, v215
	v_mul_f32_e32 v173, v173, v215
	v_mul_f32_e32 v165, v165, v8
	v_mul_f32_e32 v173, v173, v9
	v_mul_f32_e32 v165, v165, v208
	v_mul_f32_e32 v173, v173, v209
	v_cvt_pk_bf16_f32 v181, v165, v173
	v_lshlrev_b32_e32 v208, 16, v182
	v_and_b32_e32 v209, 0xffff0000, v182
	v_mul_f32_e32 v166, v166, v215
	v_mul_f32_e32 v174, v174, v215
	v_mul_f32_e32 v166, v166, v10
	v_mul_f32_e32 v174, v174, v11
	v_mul_f32_e32 v166, v166, v208
	v_mul_f32_e32 v174, v174, v209
	v_cvt_pk_bf16_f32 v182, v166, v174
	v_lshlrev_b32_e32 v208, 16, v183
	v_and_b32_e32 v209, 0xffff0000, v183
	v_mul_f32_e32 v167, v167, v215
	v_mul_f32_e32 v175, v175, v215
	v_mul_f32_e32 v167, v167, v12
	v_mul_f32_e32 v175, v175, v13
	v_mul_f32_e32 v167, v167, v208
	v_mul_f32_e32 v175, v175, v209
	v_cvt_pk_bf16_f32 v183, v167, v175
	global_store_dwordx4 v1, v[180:183], s[30:31] offset:3072
	s_add_u32 s23, s23, s21
	s_cmp_lt_u32 s23, 0x4000
	s_cbranch_scc0 .Lp5c_end
; DEV unsigned cvt_pk_bf16(float lo, float hi) { const f32x2 v = {lo, hi}; const bf16n2 r = __builtin_convertvector(v, bf16n2); return __builtin_bit_cast(unsigned, r); }
; DEV void phase5c_rec(CParams& p, int wg, int nwg) {
;     ...
;     const bf16_t* a = p.of + (long)row * 1024 + lane * 16; const bf16_t* b = p.ob + (long)row * 1024 + lane * 16;
;     const u32x4 a0 = *(const u32x4*)a, a1 = *(const u32x4*)(a + 8), b0 = *(const u32x4*)b, b1 = *(const u32x4*)(b + 8);
;     const unsigned aw[8] = {a0.x, a0.y, a0.z, a0.w, a1.x, a1.y, a1.z, a1.w}, bw[8] = {b0.x, b0.y, b0.z, b0.w, b1.x, b1.y, b1.z, b1.w};
;     float v[16]; float ss = 0.f;
; #pragma unroll
;     for (int i = 0; i < 8; ++i) { v[2 * i] = bflo(aw[i]) + bflo(bw[i]); v[2 * i + 1] = bfhi(aw[i]) + bfhi(bw[i]); ss += v[2 * i] * v[2 * i] + v[2 * i + 1] * v[2 * i + 1]; }
;     ss += __shfl_xor(ss, 1); ss += __shfl_xor(ss, 2); ss += __shfl_xor(ss, 4);
;     const float rstd = rsqrtf(ss * (1.f / DV) + EPS);
;     const bf16_t* gp = p.gate + (long)(NCTX + row) * 1024 + lane * 16;
;     const u32x4 g0 = *(const u32x4*)gp, g1 = *(const u32x4*)(gp + 8);
;     float gt[16]; gt[0] = bflo(g0.x); gt[1] = bfhi(g0.x); gt[2] = bflo(g0.y); gt[3] = bfhi(g0.y); gt[4] = bflo(g0.z); gt[5] = bfhi(g0.z); gt[6] = bflo(g0.w); gt[7] = bfhi(g0.w);
;     gt[8] = bflo(g1.x); gt[9] = bfhi(g1.x); gt[10] = bflo(g1.y); gt[11] = bfhi(g1.y); gt[12] = bflo(g1.z); gt[13] = bfhi(g1.z); gt[14] = bflo(g1.w); gt[15] = bfhi(g1.w);
;     const float* gn = p.g_norm + (lane & 7) * 16;
;     unsigned o[8];
; #pragma unroll
;     for (int j = 0; j < 8; ++j) o[j] = cvt_pk_bf16(v[2 * j] * rstd * gn[2 * j] * gt[2 * j], v[2 * j + 1] * rstd * gn[2 * j + 1] * gt[2 * j + 1]);
;     bf16_t* op = p.aout + (long)row * DM + 1024 + lane * 16;
;     *(u32x4*)op = (u32x4){o[0], o[1], o[2], o[3]}; *(u32x4*)(op + 8) = (u32x4){o[4], o[5], o[6], o[7]};
; __device__ __forceinline__ void xcd_barrier(const XcdBarrier& b) {
;     asm volatile("s_waitcnt vmcnt(0)" ::: "memory");
;     __syncthreads();
;     if (threadIdx.x == 0) {
;         unsigned* bar = b.bar;
;         __builtin_amdgcn_s_waitcnt(0);
;         unsigned nloc = b.st[0], nx = b.st[1];
;         if (nloc == 0u) { xcd_barrier_complete(bar, b.x, nloc, nx); b.st[0] = nloc; b.st[1] = nx; }
;         const unsigned old = xb_add(&bar[XB_XSUB(b.x)], 1u);
;         const unsigned gen = old / nloc;
	s_waitcnt vmcnt(14)
	v_lshlrev_b32_e32 v208, 16, v184
	v_lshlrev_b32_e32 v209, 16, v192
	v_and_b32_e32 v210, 0xffff0000, v184
	v_and_b32_e32 v211, 0xffff0000, v192
	v_add_f32_e32 v184, v208, v209
	v_add_f32_e32 v192, v210, v211
	v_lshlrev_b32_e32 v208, 16, v185
	v_lshlrev_b32_e32 v209, 16, v193
	v_and_b32_e32 v210, 0xffff0000, v185
	v_and_b32_e32 v211, 0xffff0000, v193
	v_add_f32_e32 v185, v208, v209
	v_add_f32_e32 v193, v210, v211
	v_lshlrev_b32_e32 v208, 16, v186
	v_lshlrev_b32_e32 v209, 16, v194
	v_and_b32_e32 v210, 0xffff0000, v186
	v_and_b32_e32 v211, 0xffff0000, v194
	v_add_f32_e32 v186, v208, v209
	v_add_f32_e32 v194, v210, v211
	v_lshlrev_b32_e32 v208, 16, v187
	v_lshlrev_b32_e32 v209, 16, v195
	v_and_b32_e32 v210, 0xffff0000, v187
	v_and_b32_e32 v211, 0xffff0000, v195
	v_add_f32_e32 v187, v208, v209
	v_add_f32_e32 v195, v210, v211
	v_mul_f32_e32 v212, v184, v184
	v_fmac_f32_e32 v212, v192, v192
	v_fmac_f32_e32 v212, v185, v185
	v_fmac_f32_e32 v212, v193, v193
	v_fmac_f32_e32 v212, v186, v186
	v_fmac_f32_e32 v212, v194, v194
	v_fmac_f32_e32 v212, v187, v187
	v_fmac_f32_e32 v212, v195, v195
	v_lshlrev_b32_e32 v208, 16, v188
	v_lshlrev_b32_e32 v209, 16, v196
	v_and_b32_e32 v210, 0xffff0000, v188
	v_and_b32_e32 v211, 0xffff0000, v196
	v_add_f32_e32 v188, v208, v209
	v_add_f32_e32 v196, v210, v211
	v_lshlrev_b32_e32 v208, 16, v189
	v_lshlrev_b32_e32 v209, 16, v197
	v_and_b32_e32 v210, 0xffff0000, v189
	v_and_b32_e32 v211, 0xffff0000, v197
	v_add_f32_e32 v189, v208, v209
	v_add_f32_e32 v197, v210, v211
	v_lshlrev_b32_e32 v208, 16, v190
	v_lshlrev_b32_e32 v209, 16, v198
	v_and_b32_e32 v210, 0xffff0000, v190
	v_and_b32_e32 v211, 0xffff0000, v198
	v_add_f32_e32 v190, v208, v209
	v_add_f32_e32 v198, v210, v211
	v_lshlrev_b32_e32 v208, 16, v191
	v_lshlrev_b32_e32 v209, 16, v199
	v_and_b32_e32 v210, 0xffff0000, v191
	v_and_b32_e32 v211, 0xffff0000, v199
	v_add_f32_e32 v191, v208, v209
	v_add_f32_e32 v199, v210, v211
	v_mul_f32_e32 v213, v188, v188
	v_fmac_f32_e32 v213, v196, v196
	v_fmac_f32_e32 v213, v189, v189
	v_fmac_f32_e32 v213, v197, v197
	v_fmac_f32_e32 v213, v190, v190
	v_fmac_f32_e32 v213, v198, v198
	v_fmac_f32_e32 v213, v191, v191
	v_fmac_f32_e32 v213, v199, v199
	ds_bpermute_b32 v214, v2, v212
	ds_bpermute_b32 v215, v2, v213
	s_waitcnt lgkmcnt(0)
	v_add_f32_e32 v212, v212, v214
	v_add_f32_e32 v213, v213, v215
	ds_bpermute_b32 v214, v3, v212
	ds_bpermute_b32 v215, v3, v213
	s_waitcnt lgkmcnt(0)
	v_add_f32_e32 v212, v212, v214
	v_add_f32_e32 v213, v213, v215
	ds_bpermute_b32 v214, v4, v212
	ds_bpermute_b32 v215, v4, v213
	s_waitcnt lgkmcnt(0)
	v_add_f32_e32 v212, v212, v214
	v_add_f32_e32 v213, v213, v215
	ds_bpermute_b32 v214, v5, v212
	ds_bpermute_b32 v215, v5, v213
	s_waitcnt lgkmcnt(0)
	v_add_f32_e32 v212, v212, v214
	v_add_f32_e32 v213, v213, v215
	v_mov_b32_e32 v214, 0x358637bd
	v_fmac_f32_e32 v214, 0x3c000000, v212
	v_mov_b32_e32 v215, 0x358637bd
	v_fmac_f32_e32 v215, 0x3c000000, v213
	v_rsq_f32_e32 v214, v214
	v_rsq_f32_e32 v215, v215
	s_lshl_b32 s22, s23, 12
	s_add_u32 s30, s4, s22
	s_addc_u32 s31, s5, 0
	v_lshlrev_b32_e32 v208, 16, v200
	v_and_b32_e32 v209, 0xffff0000, v200
	v_mul_f32_e32 v184, v184, v214
	v_mul_f32_e32 v192, v192, v214
	v_mul_f32_e32 v184, v184, v6
	v_mul_f32_e32 v192, v192, v7
	v_mul_f32_e32 v184, v184, v208
	v_mul_f32_e32 v192, v192, v209
	v_cvt_pk_bf16_f32 v200, v184, v192
	v_lshlrev_b32_e32 v208, 16, v201
	v_and_b32_e32 v209, 0xffff0000, v201
	v_mul_f32_e32 v185, v185, v214
	v_mul_f32_e32 v193, v193, v214
	v_mul_f32_e32 v185, v185, v8
	v_mul_f32_e32 v193, v193, v9
	v_mul_f32_e32 v185, v185, v208
	v_mul_f32_e32 v193, v193, v209
	v_cvt_pk_bf16_f32 v201, v185, v193
	v_lshlrev_b32_e32 v208, 16, v202
	v_and_b32_e32 v209, 0xffff0000, v202
	v_mul_f32_e32 v186, v186, v214
	v_mul_f32_e32 v194, v194, v214
	v_mul_f32_e32 v186, v186, v10
	v_mul_f32_e32 v194, v194, v11
	v_mul_f32_e32 v186, v186, v208
	v_mul_f32_e32 v194, v194, v209
	v_cvt_pk_bf16_f32 v202, v186, v194
	v_lshlrev_b32_e32 v208, 16, v203
	v_and_b32_e32 v209, 0xffff0000, v203
	v_mul_f32_e32 v187, v187, v214
	v_mul_f32_e32 v195, v195, v214
	v_mul_f32_e32 v187, v187, v12
	v_mul_f32_e32 v195, v195, v13
	v_mul_f32_e32 v187, v187, v208
	v_mul_f32_e32 v195, v195, v209
	v_cvt_pk_bf16_f32 v203, v187, v195
	global_store_dwordx4 v1, v[200:203], s[30:31] offset:2048
	v_lshlrev_b32_e32 v208, 16, v204
	v_and_b32_e32 v209, 0xffff0000, v204
	v_mul_f32_e32 v188, v188, v215
	v_mul_f32_e32 v196, v196, v215
	v_mul_f32_e32 v188, v188, v6
	v_mul_f32_e32 v196, v196, v7
	v_mul_f32_e32 v188, v188, v208
	v_mul_f32_e32 v196, v196, v209
	v_cvt_pk_bf16_f32 v204, v188, v196
	v_lshlrev_b32_e32 v208, 16, v205
	v_and_b32_e32 v209, 0xffff0000, v205
	v_mul_f32_e32 v189, v189, v215
	v_mul_f32_e32 v197, v197, v215
	v_mul_f32_e32 v189, v189, v8
	v_mul_f32_e32 v197, v197, v9
	v_mul_f32_e32 v189, v189, v208
	v_mul_f32_e32 v197, v197, v209
	v_cvt_pk_bf16_f32 v205, v189, v197
	v_lshlrev_b32_e32 v208, 16, v206
	v_and_b32_e32 v209, 0xffff0000, v206
	v_mul_f32_e32 v190, v190, v215
	v_mul_f32_e32 v198, v198, v215
	v_mul_f32_e32 v190, v190, v10
	v_mul_f32_e32 v198, v198, v11
	v_mul_f32_e32 v190, v190, v208
	v_mul_f32_e32 v198, v198, v209
	v_cvt_pk_bf16_f32 v206, v190, v198
	v_lshlrev_b32_e32 v208, 16, v207
	v_and_b32_e32 v209, 0xffff0000, v207
	v_mul_f32_e32 v191, v191, v215
	v_mul_f32_e32 v199, v199, v215
	v_mul_f32_e32 v191, v191, v12
	v_mul_f32_e32 v199, v199, v13
	v_mul_f32_e32 v191, v191, v208
	v_mul_f32_e32 v199, v199, v209
	v_cvt_pk_bf16_f32 v207, v191, v199
	global_store_dwordx4 v1, v[204:207], s[30:31] offset:3072
	s_lshl_b32 s22, s21, 3
	s_add_u32 s20, s20, s22
	s_cmp_lt_u32 s20, 0x4000
	s_cbranch_scc1 .Lp5c_chunk
.Lp5c_end:
.LBB0_1186:
	s_or_b64 exec, exec, s[8:9]
	s_waitcnt vmcnt(0)
	s_barrier
	s_and_saveexec_b64 s[4:5], s[40:41]
	s_cbranch_execz .LBB0_1238
	s_add_i32 s3, 0, 0x27ff0
	v_mov_b32_e32 v1, s3
	s_waitcnt vmcnt(0) expcnt(0) lgkmcnt(0)
	ds_read_b32 v3, v1
	s_add_i32 s3, 0, 0x27ff4
	v_mov_b32_e32 v1, s3
	ds_read_b32 v1, v1
	s_waitcnt lgkmcnt(1)
	v_cmp_ne_u32_e32 vcc, 0, v3
	s_cbranch_vccnz .LBB0_1202
	s_load_dwordx2 s[10:11], s[48:49], 0x4
	s_add_u32 s6, s42, 0x1000
	s_addc_u32 s7, s43, 0
	s_add_u32 s8, s42, 0x1100
	s_addc_u32 s9, s43, 0
	s_waitcnt lgkmcnt(0)
	s_mul_i32 s3, s10, s33
	s_add_u32 s10, s42, 0x1200
	s_mul_i32 s3, s3, s11
	s_addc_u32 s11, s43, 0
	s_add_u32 s12, s42, 0x1300
	s_addc_u32 s13, s43, 0
	s_mov_b32 s20, 1
	v_mov_b32_e32 v17, 0
	s_branch .LBB0_1190
